# v27 + 19 remaining provably-dead s_waitcnt lgkmcnt(0) removed (whole kernel)
# baseline (speedup 1.0000x reference)
; #define LAS __attribute__((address_space(3)))
; __device__ __forceinline__ unsigned xb_add(unsigned* p, unsigned v) { return __hip_atomic_fetch_add(p, v, __ATOMIC_RELAXED, __HIP_MEMORY_SCOPE_AGENT); }
; __device__ __forceinline__ unsigned xb_xcc_id() { return (unsigned)__builtin_amdgcn_s_getreg((3 << 11) | 20) & 0xFu; }
; #define KWS (kargs()->ws)
; __device__ __forceinline__ XcdBarrier xcd_barrier_post(unsigned* bar, volatile LAS unsigned* st) {
;     XcdBarrier b; b.bar = bar; b.x = xb_xcc_id(); b.st = st;
;     if (threadIdx.x == 0) (void)xb_add(&bar[XB_XCNT(b.x)], 1u);
;     return b;
; __global__ void __launch_bounds__(512, 2) mega(Ptrs Pdummy) {
;     extern __shared__ __attribute__((aligned(16))) unsigned char lds_raw[];
;     LAS unsigned char* lds = (LAS unsigned char*)lds_raw;
;     const int G = (int)gridDim.x, c = (int)blockIdx.x, wbase = __builtin_amdgcn_readfirstlane((int)threadIdx.x) & ~63;
;     { volatile LAS unsigned* MISC0 = (volatile LAS unsigned*)(lds + LDSCTL_OFF); if (threadIdx.x < 64) MISC0[threadIdx.x] = 0u; }
;     __syncthreads();
;     (void)xcd_barrier_post((unsigned*)(KWS + WS_CTL) + CW_BAR, (volatile LAS unsigned*)(lds + LDSCTL_OFF) + 8);
_Z4mega4Ptrs:
	s_mov_b64 s[88:89], s[0:1]
	s_load_dword s60, s[0:1], 0x100
	s_load_dwordx2 s[100:101], s[0:1], 0xf8
	s_load_dwordx4 s[4:7], s[0:1], 0xc0
	s_load_dwordx2 s[8:9], s[0:1], 0xd0
	s_load_dwordx2 s[10:11], s[0:1], 0x90
	s_waitcnt lgkmcnt(0)
	v_writelane_b32 v255, s4, 49
	v_writelane_b32 v255, s5, 50
	v_writelane_b32 v255, s6, 51
	v_writelane_b32 v255, s7, 52
	v_writelane_b32 v255, s8, 53
	v_writelane_b32 v255, s9, 54
	v_writelane_b32 v255, s10, 55
	v_writelane_b32 v255, s11, 56
	s_add_u32 s0, s88, 0x100
	s_addc_u32 s1, s89, 0
	s_mov_b32 s92, s2
	v_writelane_b32 v255, s0, 0
	v_cmp_gt_u32_e32 vcc, 64, v0
	s_nop 0
	v_writelane_b32 v255, s1, 1
	v_readfirstlane_b32 s0, v0
	s_and_saveexec_b64 s[2:3], vcc
	v_lshl_add_u32 v1, v0, 2, 0
	v_add_u32_e32 v1, 0x20000, v1
	v_mov_b32_e32 v2, 0
	ds_write_b32 v1, v2
	s_or_b64 exec, exec, s[2:3]
	s_mov_b64 s[4:5], s[88:89]
	s_waitcnt lgkmcnt(0)
	s_barrier
	s_getreg_b32 s1, hwreg(HW_REG_XCC_ID, 0, 4)
	v_cmp_eq_u32_e32 vcc, 0, v0
	s_and_saveexec_b64 s[2:3], vcc
	s_cbranch_execz .LBB0_5
	s_mov_b64 s[6:7], exec
	v_mbcnt_lo_u32_b32 v0, s6, 0
	v_mbcnt_hi_u32_b32 v0, s7, v0
	v_cmp_eq_u32_e32 vcc, 0, v0
	s_and_b64 s[8:9], exec, vcc
	s_mov_b64 exec, s[8:9]
	s_cbranch_execz .LBB0_5
	s_mov_b64 s[4:5], s[100:101]
	s_lshl_b32 s1, s1, 8
	s_and_b32 s1, s1, 0xf00
	v_mov_b32_e32 v0, 0x4000
	s_add_u32 s4, s4, s1
	s_addc_u32 s5, s5, 0
	s_bcnt1_i32_b64 s1, s[6:7]
	v_mov_b32_e32 v1, s1
	global_atomic_add v0, v1, s[4:5] offset:1024

; #define LAS __attribute__((address_space(3)))
; __device__ __forceinline__ CJob moe_job(KP P, int j2, int j) {
;     CJob jb; jb.pad = 0; jb.gain = nullptr; jb.mode = 0; jb.fp8 = MOE_FP8 ? 1 : 0; jb.wscale = 1.f; jb.col0 = 0; const int e = j / 3, k = j % 3;
;     if (k < 2) { jb.W = P->in[24 + k] + ((size_t)j2 * NEXP + e) * DM * DFF; jb.gain = P->in[18] + (2 * j2 + 1) * DM; jb.dst = (bf16*)(P->ws + WS_W13E + (size_t)e * 2 * DFF * DM * (MOE_FP8 ? 1 : 2)); jb.K = DM; jb.N = DFF; jb.mode = 4 + k; jb.wscale = MOE_FP8 ? W13_SCALE : 1.f; }
;     else { jb.W = P->in[26] + ((size_t)j2 * NEXP + e) * DFF * DM; jb.dst = (bf16*)(P->ws + WS_W2E + (size_t)e * DM * DFF * (MOE_FP8 ? 1 : 2)); jb.K = DFF; jb.N = DM; jb.wscale = MOE_FP8 ? W2_SCALE : 1.f; }
;     jb.ldw = jb.N;
; __device__ __forceinline__ void conv_moe_layer(KP P, int j2, LAS float* scr, int gw, int ngw, int lane) {
;     constexpr int IT = (DM / 64) * (DFF / 32), NT = 24 * IT;
;     int fl = gw; if (fl >= NT) return;
;     CJob jb = moe_job(P, j2, fl / IT); f32x4 v[8]; conv_load(jb, fl % IT, lane, v);
.LBB0_509:
	s_lshl_b32 s6, s16, 11
	s_andn2_b64 vcc, exec, s[2:3]
	s_mov_b32 s7, s40
	s_cbranch_vccnz .LBB0_511
	s_ashr_i32 s19, s18, 31
	s_lshl_b32 s3, s18, 1
	s_add_i32 s3, s3, 49
	v_readlane_b32 s2, v255, s3
	s_add_i32 s3, s3, 1
	v_readlane_b32 s3, v255, s3
	s_mul_i32 s9, s13, 0xe00000
	s_mul_hi_i32 s8, s13, 0xe00000
	s_mul_hi_i32 s10, s13, 0x700000
	s_mul_i32 s13, s13, 0x700000
	s_waitcnt lgkmcnt(0)
	s_add_u32 s2, s2, s9
	s_addc_u32 s3, s3, s8
	s_add_u32 s14, s2, s12
	s_addc_u32 s15, s3, s1
	v_readlane_b32 s2, v255, 55
	v_readlane_b32 s3, v255, 56
	s_lshl_b64 s[8:9], s[6:7], 2
	s_mov_b32 s17, s40
	s_mov_b32 s24, 0x42800000
	s_movk_i32 s33, 0xe00
	s_add_u32 s2, s2, s8
	s_addc_u32 s3, s3, s9
	s_mov_b64 s[8:9], s[100:101]
	s_add_u32 s2, s2, 0x1000
	s_addc_u32 s3, s3, 0
	s_add_u32 s8, s8, s13
	s_addc_u32 s9, s9, s10
	s_add_u32 s10, s8, 0x7a00000
	s_addc_u32 s11, s9, 0
	s_add_i32 s30, s18, 4
	s_lshl_b64 s[8:9], s[16:17], 3
	s_movk_i32 s13, 0x400
	s_branch .LBB0_512

; __device__ __forceinline__ CJob moe_job(KP P, int j2, int j) {
;     CJob jb; jb.pad = 0; jb.gain = nullptr; jb.mode = 0; jb.fp8 = MOE_FP8 ? 1 : 0; jb.wscale = 1.f; jb.col0 = 0; const int e = j / 3, k = j % 3;
;     if (k < 2) { jb.W = P->in[24 + k] + ((size_t)j2 * NEXP + e) * DM * DFF; jb.gain = P->in[18] + (2 * j2 + 1) * DM; jb.dst = (bf16*)(P->ws + WS_W13E + (size_t)e * 2 * DFF * DM * (MOE_FP8 ? 1 : 2)); jb.K = DM; jb.N = DFF; jb.mode = 4 + k; jb.wscale = MOE_FP8 ? W13_SCALE : 1.f; }
;     else { jb.W = P->in[26] + ((size_t)j2 * NEXP + e) * DFF * DM; jb.dst = (bf16*)(P->ws + WS_W2E + (size_t)e * DM * DFF * (MOE_FP8 ? 1 : 2)); jb.K = DFF; jb.N = DM; jb.wscale = MOE_FP8 ? W2_SCALE : 1.f; }
;     jb.ldw = jb.N;
; __device__ __forceinline__ void conv_moe_layer(KP P, int j2, LAS float* scr, int gw, int ngw, int lane) {
;     ...
;     for (;;) { const int nx = fl + ngw; const bool has = nx < NT; CJob jn = jb; f32x4 w[8];
;         if (has) { jn = moe_job(P, j2, nx / IT); conv_load(jn, nx % IT, lane, w); }
.LBB0_517:
	s_andn2_b64 vcc, exec, s[14:15]
	s_cbranch_vccnz .LBB0_519
	s_ashr_i32 s23, s22, 31
	s_lshl_b32 s15, s22, 1
	s_add_i32 s15, s15, 49
	v_readlane_b32 s14, v255, s15
	s_add_i32 s15, s15, 1
	v_readlane_b32 s15, v255, s15
	s_mul_i32 s17, s26, 0xe00000
	s_mul_hi_i32 s16, s26, 0xe00000
	s_mul_hi_i32 s23, s26, 0x700000
	s_mul_i32 s26, s26, 0x700000
	s_waitcnt lgkmcnt(0)
	s_add_u32 s14, s14, s17
	s_addc_u32 s15, s15, s16
	s_add_u32 s20, s14, s12
	s_addc_u32 s21, s15, s1
	v_readlane_b32 s14, v255, 55
	v_readlane_b32 s15, v255, 56
	s_lshl_b64 s[16:17], s[6:7], 2
	s_mov_b32 s27, 0x42800000
	s_movk_i32 s28, 0xe00
	s_movk_i32 s29, 0x400
	s_add_u32 s14, s14, s16
	s_addc_u32 s15, s15, s17
	s_mov_b64 s[16:17], s[100:101]
	s_add_u32 s14, s14, 0x1000
	s_addc_u32 s15, s15, 0
	s_add_u32 s16, s16, s26
	s_addc_u32 s17, s17, s23
	s_add_u32 s16, s16, 0x7a00000
	s_addc_u32 s17, s17, 0
	s_add_i32 s26, s22, 4
	s_branch .LBB0_520

; #define LAS __attribute__((address_space(3)))
; __device__ __forceinline__ unsigned cvt_pk_bf16(float lo, float hi) { unsigned r; asm volatile("v_cvt_pk_bf16_f32 %0, %1, %2" : "=v"(r) : "v"(lo), "v"(hi)); return r; }
; __device__ __forceinline__ void conv_finish(const CJob& jb, LAS float* scr, int item, int lane, const f32x4 (&v)[8]) {
;     ...
;     for (int j = 0; j < 4; ++j) { const int n = (lane >> 3) + 8 * j; const LAS float* s = scr + (8 * c) * 33 + n;
;         u32x4 o; o.x = cvt_pk_bf16(s[0 * 33] * g0.x, s[1 * 33] * g0.y); o.y = cvt_pk_bf16(s[2 * 33] * g0.z, s[3 * 33] * g0.w); o.z = cvt_pk_bf16(s[4 * 33] * g1.x, s[5 * 33] * g1.y); o.w = cvt_pk_bf16(s[6 * 33] * g1.z, s[7 * 33] * g1.w);
;         const int nn = n0 + n; int row = nn;
;         if (jb.mode == 3) { const int w = nn & 255; row = (nn & ~255) + ((w >> 5) & 1) * 128 + (w >> 6) * 32 + (w & 31); }
;         else if (jb.mode >= 4) { const int r = nn & 127; row = (nn >> 7) * 256 + ((r >> 2) & 1) * 128 + (r >> 5) * 32 + ((r >> 3) & 3) * 8 + (jb.mode == 5 ? 4 : 0) + (r & 3); }
;         if (jb.fp8) { const float ws_ = jb.wscale; u32x2 o8; o8.x = pk4_fp8(s[0 * 33] * g0.x * ws_, s[1 * 33] * g0.y * ws_, s[2 * 33] * g0.z * ws_, s[3 * 33] * g0.w * ws_);
;             o8.y = pk4_fp8(s[4 * 33] * g1.x * ws_, s[5 * 33] * g1.y * ws_, s[6 * 33] * g1.z * ws_, s[7 * 33] * g1.w * ws_); *(u32x2*)((unsigned char*)jb.dst + (size_t)row * jb.K + k0 + 8 * c) = o8; }
;         else *(u32x4*)(jb.dst + (size_t)row * jb.K + k0 + 8 * c) = o; }
;     asm volatile("s_waitcnt lgkmcnt(0)" ::: "memory");
; }
; __device__ __forceinline__ void conv_moe_layer(KP P, int j2, LAS float* scr, int gw, int ngw, int lane) {
;     ...
;         conv_finish(jb, scr, fl % IT, lane, v);
;         if (!has) break;
;         jb = jn; fl = nx;
; #pragma unroll
;         for (int i = 0; i < 8; ++i) v[i] = w[i]; }
.LBB0_540:
	ds_read2_b32 v[34:35], v79 offset0:24 offset1:57
	s_andn2_b64 vcc, exec, s[18:19]
	s_waitcnt lgkmcnt(0)
	v_mul_f32_e32 v32, v68, v34
	v_mul_f32_e32 v34, v69, v35
	v_mul_f32_e32 v36, s24, v34
	ds_read2_b32 v[34:35], v79 offset0:90 offset1:123
	v_mul_f32_e32 v32, s24, v32
	s_waitcnt lgkmcnt(0)
	v_mul_f32_e32 v34, v70, v34
	v_mul_f32_e32 v37, s24, v34
	v_mul_f32_e32 v34, v71, v35
	v_mul_f32_e32 v35, s24, v34
	v_med3_f32 v34, v32, s49, v254
	v_med3_f32 v32, v36, s49, v254
	v_cvt_pk_fp8_f32 v34, v34, v32
	v_med3_f32 v36, v37, s49, v254
	v_med3_f32 v35, v35, s49, v254
	v_cvt_pk_fp8_f32 v34, v36, v35 op_sel:[0,0,1]
	ds_read2_b32 v[36:37], v79 offset0:156 offset1:189
	s_waitcnt lgkmcnt(0)
	v_mul_f32_e32 v32, v64, v36
	v_mul_f32_e32 v35, v65, v37
	ds_read2_b32 v[36:37], v79 offset0:222 offset1:255
	v_mul_f32_e32 v38, s24, v35
	v_mul_f32_e32 v32, s24, v32
	s_waitcnt lgkmcnt(0)
	v_mul_f32_e32 v35, v66, v36
	v_mul_f32_e32 v36, s24, v35
	v_mul_f32_e32 v35, v67, v37
	v_mul_f32_e32 v37, s24, v35
	v_med3_f32 v35, v32, s49, v254
	v_med3_f32 v32, v38, s49, v254
	v_cvt_pk_fp8_f32 v35, v35, v32
	v_med3_f32 v36, v36, s49, v254
	v_med3_f32 v37, v37, s49, v254
	v_ashrrev_i32_e32 v38, 31, v33
	v_cvt_pk_fp8_f32 v35, v36, v37 op_sel:[0,0,1]
	v_mov_b64_e32 v[36:37], s[10:11]
	v_mad_u64_u32 v[32:33], s[2:3], v33, s13, v[36:37]
	v_mov_b32_e32 v36, v33
	v_mad_u64_u32 v[36:37], s[2:3], v38, s13, v[36:37]
	v_mov_b32_e32 v33, v36
	v_lshl_add_u64 v[32:33], v[32:33], 0, s[20:21]
	v_lshl_add_u64 v[32:33], v[32:33], 0, v[72:73]
	global_store_dwordx2 v[32:33], v[34:35], off
	s_mov_b64 s[2:3], -1
	s_cbranch_vccnz .LBB0_513
	s_mov_b64 s[2:3], 0
	v_mov_b32_e32 v35, v27
	v_mov_b32_e32 v34, v26
	v_mov_b32_e32 v33, v25
	v_mov_b32_e32 v32, v24
	v_mov_b32_e32 v39, v31
	v_mov_b32_e32 v38, v30
	v_mov_b32_e32 v37, v29
	v_mov_b32_e32 v36, v28
	v_mov_b32_e32 v43, v19
	v_mov_b32_e32 v42, v18
	v_mov_b32_e32 v41, v17
	v_mov_b32_e32 v40, v16
	v_mov_b32_e32 v47, v23
	v_mov_b32_e32 v46, v22
	v_mov_b32_e32 v45, v21
	v_mov_b32_e32 v44, v20
	v_mov_b32_e32 v51, v11
	v_mov_b32_e32 v50, v10
	v_mov_b32_e32 v49, v9
	v_mov_b32_e32 v48, v8
	v_mov_b32_e32 v55, v15
	v_mov_b32_e32 v54, v14
	v_mov_b32_e32 v53, v13
	v_mov_b32_e32 v52, v12
	v_mov_b32_e32 v59, v3
	v_mov_b32_e32 v58, v2
	v_mov_b32_e32 v57, v1
	v_mov_b32_e32 v56, v0
	v_mov_b32_e32 v63, v7
	v_mov_b32_e32 v62, v6
	v_mov_b32_e32 v61, v5
	v_mov_b32_e32 v60, v4
	s_branch .LBB0_513

; __device__ __forceinline__ void attn_phase(LAS unsigned char* lds, const bf16* U, bf16* YA, const float* sinks, const float* rel_bias, int G, int c, int wbase, int y8) {
;     ...
;     for (int L = c; L < BATCH * 32 * 4; L += G) {
;     ...
;             asm volatile("s_waitcnt lgkmcnt(0)" ::: "memory");
;         }
;         __syncthreads();
;     }
.LBB0_546:
	s_waitcnt lgkmcnt(0)
	s_add_i32 s33, s33, s1
	s_cmpk_lt_i32 s33, 0x400
	s_barrier
	s_cbranch_scc0 .LBB0_589

; #define LAS __attribute__((address_space(3)))
; __device__ __forceinline__ int crow(int r, int hi) { return (r & 3) + 8 * (r >> 2) + 4 * hi; }
; __device__ __forceinline__ int crow(int r, int hi) { return (r & 3) + 8 * (r >> 2) + 4 * hi; }
; __device__ __forceinline__ void attn_phase(LAS unsigned char* lds, const bf16* U, bf16* YA, const float* sinks, const float* rel_bias, int G, int c, int wbase, int y8) {
;     ...
;         for (int qt = 0; qt < 2; ++qt) {
;             const int iq0 = 64 * qh + 32 * qt, kt0 = iq0 >> 5; const size_t mq = mq0 + 32 * qt;
;             f32x16 p[5];
; #pragma unroll
;             for (int jt = 0; jt < 5; ++jt) { f32x16 a = {};
; #pragma unroll
;                 for (int d0 = 0; d0 < 4; ++d0) { const bf16x8 kf = *(const LAS bf16x8*)(lds + KIMG + (2 * d0 + hi) * 4096 + (32 * (kt0 + jt) + r32) * 16); a = __builtin_amdgcn_mfma_f32_32x32x16_bf16(kf, qf[qt][d0], a, 0, 0, 0); }
;                 p[jt] = a; }
;             float mx = sink2;
; #pragma unroll
;             for (int jt = 0; jt < 5; ++jt)
; #pragma unroll
;                 for (int r = 0; r < 16; ++r) { float s = p[jt][r] + bt[32 * jt + (r & 3) + 8 * (r >> 2)];
;                     if (n == 0) { if (32 * (kt0 + jt) + crow(r, hi) < 128) s = -1.0e30f; }
;                     p[jt][r] = s; mx = fmaxf(mx, s); }
.LBB0_568:
	s_waitcnt lgkmcnt(0)
	ds_read_b128 v[0:3], v152
	v_add_u32_e32 v105, s57, v123
	s_waitcnt lgkmcnt(0)
	v_mfma_f32_32x32x16_bf16 v[64:79], v[0:3], v[92:95], 0
	ds_read_b128 v[0:3], v152 offset:8192
	s_waitcnt lgkmcnt(0)
	v_mfma_f32_32x32x16_bf16 v[64:79], v[0:3], v[88:91], v[64:79]
	ds_read_b128 v[0:3], v152 offset:16384
	s_waitcnt lgkmcnt(0)
	v_mfma_f32_32x32x16_bf16 v[64:79], v[0:3], v[84:87], v[64:79]
	ds_read_b128 v[0:3], v152 offset:24576
	s_waitcnt lgkmcnt(0)
	v_mfma_f32_32x32x16_bf16 v[64:79], v[0:3], v[80:83], v[64:79]
	ds_read_b128 v[0:3], v153
	s_waitcnt lgkmcnt(0)
	v_mfma_f32_32x32x16_bf16 v[48:63], v[0:3], v[92:95], 0
	ds_read_b128 v[0:3], v153 offset:8192
	s_waitcnt lgkmcnt(0)
	v_mfma_f32_32x32x16_bf16 v[48:63], v[0:3], v[88:91], v[48:63]
	ds_read_b128 v[0:3], v153 offset:16384
	s_waitcnt lgkmcnt(0)
	v_mfma_f32_32x32x16_bf16 v[48:63], v[0:3], v[84:87], v[48:63]
	ds_read_b128 v[0:3], v153 offset:24576
	s_waitcnt lgkmcnt(0)
	v_mfma_f32_32x32x16_bf16 v[48:63], v[0:3], v[80:83], v[48:63]
	ds_read_b128 v[0:3], v154
	s_waitcnt lgkmcnt(0)
	v_mfma_f32_32x32x16_bf16 v[32:47], v[0:3], v[92:95], 0
	ds_read_b128 v[0:3], v154 offset:8192
	s_waitcnt lgkmcnt(0)
	v_mfma_f32_32x32x16_bf16 v[32:47], v[0:3], v[88:91], v[32:47]
	ds_read_b128 v[0:3], v154 offset:16384
	s_waitcnt lgkmcnt(0)
	v_mfma_f32_32x32x16_bf16 v[32:47], v[0:3], v[84:87], v[32:47]
	ds_read_b128 v[0:3], v154 offset:24576
	s_waitcnt lgkmcnt(0)
	v_mfma_f32_32x32x16_bf16 v[32:47], v[0:3], v[80:83], v[32:47]
	ds_read_b128 v[0:3], v155
	s_waitcnt lgkmcnt(0)
	v_mfma_f32_32x32x16_bf16 v[16:31], v[0:3], v[92:95], 0
	ds_read_b128 v[0:3], v155 offset:8192
	s_waitcnt lgkmcnt(0)
	v_mfma_f32_32x32x16_bf16 v[16:31], v[0:3], v[88:91], v[16:31]
	ds_read_b128 v[0:3], v155 offset:16384
	s_waitcnt lgkmcnt(0)
	v_mfma_f32_32x32x16_bf16 v[16:31], v[0:3], v[84:87], v[16:31]
	ds_read_b128 v[0:3], v155 offset:24576
	s_waitcnt lgkmcnt(0)
	v_mfma_f32_32x32x16_bf16 v[16:31], v[0:3], v[80:83], v[16:31]
	ds_read_b128 v[0:3], v105
	s_waitcnt lgkmcnt(0)
	v_mfma_f32_32x32x16_bf16 v[0:15], v[0:3], v[92:95], 0
	ds_read_b128 v[92:95], v105 offset:8192
	s_waitcnt lgkmcnt(0)
	v_mfma_f32_32x32x16_bf16 v[0:15], v[92:95], v[88:91], v[0:15]
	ds_read_b128 v[88:91], v105 offset:16384
	s_waitcnt lgkmcnt(0)
	v_mfma_f32_32x32x16_bf16 v[0:15], v[88:91], v[84:87], v[0:15]
	ds_read_b128 v[84:87], v105 offset:24576
	s_waitcnt lgkmcnt(0)
	v_mfma_f32_32x32x16_bf16 v[0:15], v[84:87], v[80:83], v[0:15]
	ds_read2_b32 v[80:81], v121 offset0:31 offset1:32
	ds_read2_b32 v[82:83], v121 offset0:33 offset1:34
	v_mov_b32_e32 v86, 0xf149f2ca
	s_waitcnt lgkmcnt(1)
	v_add_f32_e32 v64, v64, v80
	v_cndmask_b32_e64 v80, v64, v86, s[4:5]
	v_add_f32_e32 v64, v65, v81
	s_waitcnt lgkmcnt(0)
	v_add_f32_e32 v65, v66, v82
	v_cndmask_b32_e64 v66, v65, v86, s[4:5]
	v_add_f32_e32 v65, v67, v83
	ds_read2_b32 v[82:83], v121 offset0:39 offset1:40
	v_cndmask_b32_e64 v64, v64, v86, s[4:5]
	v_max3_f32 v81, v151, v80, v64
	v_cndmask_b32_e64 v65, v65, v86, s[4:5]
	v_max3_f32 v81, v81, v66, v65
	s_waitcnt lgkmcnt(0)
	v_add_f32_e32 v67, v68, v82
	v_cndmask_b32_e64 v68, v67, v86, s[4:5]
	v_add_f32_e32 v67, v69, v83
	ds_read2_b32 v[82:83], v121 offset0:41 offset1:42
	v_cndmask_b32_e64 v67, v67, v86, s[4:5]
	v_max3_f32 v69, v81, v68, v67
	s_waitcnt lgkmcnt(0)
	v_add_f32_e32 v70, v70, v82
	v_cndmask_b32_e64 v81, v70, v86, s[4:5]
	v_add_f32_e32 v70, v71, v83
	ds_read2_b32 v[82:83], v121 offset0:47 offset1:48
	v_cndmask_b32_e64 v70, v70, v86, s[4:5]
	v_max3_f32 v84, v69, v81, v70
	s_waitcnt lgkmcnt(0)
	v_add_f32_e32 v69, v72, v82
	v_cndmask_b32_e64 v71, v69, v86, s[4:5]
	v_add_f32_e32 v69, v73, v83
	ds_read2_b32 v[82:83], v121 offset0:49 offset1:50
	v_cndmask_b32_e64 v69, v69, v86, s[4:5]
	v_max3_f32 v84, v84, v71, v69
	s_waitcnt lgkmcnt(0)
	v_add_f32_e32 v72, v74, v82
	v_cndmask_b32_e64 v73, v72, v86, s[4:5]
	v_add_f32_e32 v72, v75, v83
	ds_read2_b32 v[82:83], v121 offset0:55 offset1:56
	v_cndmask_b32_e64 v72, v72, v86, s[4:5]
	v_max3_f32 v84, v84, v73, v72
	s_waitcnt lgkmcnt(0)
	v_add_f32_e32 v74, v76, v82
	v_cndmask_b32_e64 v75, v74, v86, s[4:5]
	v_add_f32_e32 v74, v77, v83
	ds_read2_b32 v[76:77], v121 offset0:57 offset1:58
	v_cndmask_b32_e64 v74, v74, v86, s[4:5]
	v_max3_f32 v82, v84, v75, v74
	s_waitcnt lgkmcnt(0)
	v_add_f32_e32 v76, v78, v76
	v_cndmask_b32_e64 v78, v76, v86, s[4:5]
	v_add_f32_e32 v76, v79, v77
	v_cndmask_b32_e64 v76, v76, v86, s[4:5]
	v_max3_f32 v79, v82, v78, v76
	ds_read2_b32 v[82:83], v121 offset0:63 offset1:64
	s_waitcnt lgkmcnt(0)
	v_add_f32_e32 v48, v48, v82
	v_cndmask_b32_e64 v77, v48, v86, s[6:7]
	v_add_f32_e32 v48, v49, v83
	ds_read2_b32 v[82:83], v121 offset0:65 offset1:66
	v_cndmask_b32_e64 v48, v48, v86, s[6:7]
	v_max3_f32 v79, v79, v77, v48
	s_waitcnt lgkmcnt(0)
	v_add_f32_e32 v49, v50, v82
	v_cndmask_b32_e64 v50, v49, v86, s[6:7]
	v_add_f32_e32 v49, v51, v83
	ds_read2_b32 v[82:83], v121 offset0:71 offset1:72
	v_cndmask_b32_e64 v49, v49, v86, s[6:7]
	v_max3_f32 v79, v79, v50, v49
	s_waitcnt lgkmcnt(0)
	v_add_f32_e32 v51, v52, v82
	v_cndmask_b32_e64 v52, v51, v86, s[6:7]
	v_add_f32_e32 v51, v53, v83
	ds_read2_b32 v[82:83], v121 offset0:73 offset1:74
	v_cndmask_b32_e64 v51, v51, v86, s[6:7]
	v_max3_f32 v53, v79, v52, v51
	s_waitcnt lgkmcnt(0)
	v_add_f32_e32 v54, v54, v82
	v_cndmask_b32_e64 v79, v54, v86, s[6:7]
	v_add_f32_e32 v54, v55, v83
	ds_read2_b32 v[82:83], v121 offset0:79 offset1:80
	v_cndmask_b32_e64 v54, v54, v86, s[6:7]
	v_max3_f32 v84, v53, v79, v54
	s_waitcnt lgkmcnt(0)
	v_add_f32_e32 v53, v56, v82
	v_cndmask_b32_e64 v55, v53, v86, s[6:7]
	v_add_f32_e32 v53, v57, v83
	ds_read2_b32 v[82:83], v121 offset0:81 offset1:82
	v_cndmask_b32_e64 v53, v53, v86, s[6:7]
	v_max3_f32 v84, v84, v55, v53
	s_waitcnt lgkmcnt(0)
; __device__ __forceinline__ int crow(int r, int hi) { return (r & 3) + 8 * (r >> 2) + 4 * hi; }
; __device__ __forceinline__ int crow(int r, int hi) { return (r & 3) + 8 * (r >> 2) + 4 * hi; }
; __device__ __forceinline__ void attn_phase(LAS unsigned char* lds, const bf16* U, bf16* YA, const float* sinks, const float* rel_bias, int G, int c, int wbase, int y8) {
;     ...
;             float mx = sink2;
; #pragma unroll
;             for (int jt = 0; jt < 5; ++jt)
; #pragma unroll
;                 for (int r = 0; r < 16; ++r) { float s = p[jt][r] + bt[32 * jt + (r & 3) + 8 * (r >> 2)];
;                     if (n == 0) { if (32 * (kt0 + jt) + crow(r, hi) < 128) s = -1.0e30f; }
;                     p[jt][r] = s; mx = fmaxf(mx, s); }
	v_add_f32_e32 v56, v58, v82
	v_cndmask_b32_e64 v57, v56, v86, s[6:7]
	v_add_f32_e32 v56, v59, v83
	ds_read2_b32 v[82:83], v121 offset0:87 offset1:88
	v_cndmask_b32_e64 v56, v56, v86, s[6:7]
	v_max3_f32 v84, v84, v57, v56
	s_waitcnt lgkmcnt(0)
	v_add_f32_e32 v58, v60, v82
	v_cndmask_b32_e64 v59, v58, v86, s[6:7]
	v_add_f32_e32 v58, v61, v83
	ds_read2_b32 v[60:61], v121 offset0:89 offset1:90
	v_cndmask_b32_e64 v58, v58, v86, s[6:7]
	v_max3_f32 v82, v84, v59, v58
	ds_read2_b32 v[84:85], v121 offset0:111 offset1:112
	s_waitcnt lgkmcnt(1)
	v_add_f32_e32 v60, v62, v60
	v_cndmask_b32_e64 v62, v60, v86, s[6:7]
	v_add_f32_e32 v60, v63, v61
	v_cndmask_b32_e64 v60, v60, v86, s[6:7]
	v_max3_f32 v63, v82, v62, v60
	ds_read2_b32 v[82:83], v121 offset0:95 offset1:96
	s_waitcnt lgkmcnt(0)
	v_add_f32_e32 v32, v32, v82
	v_cndmask_b32_e64 v61, v32, v86, s[6:7]
	v_add_f32_e32 v32, v33, v83
	ds_read2_b32 v[82:83], v121 offset0:97 offset1:98
	v_cndmask_b32_e64 v33, v32, v86, s[6:7]
	v_max3_f32 v32, v63, v61, v33
	s_waitcnt lgkmcnt(0)
	v_add_f32_e32 v34, v34, v82
	v_cndmask_b32_e64 v63, v34, v86, s[6:7]
	v_add_f32_e32 v34, v35, v83
	ds_read2_b32 v[82:83], v121 offset0:103 offset1:104
	v_cndmask_b32_e64 v34, v34, v86, s[6:7]
	v_max3_f32 v32, v32, v63, v34
	s_waitcnt lgkmcnt(0)
	v_add_f32_e32 v35, v36, v82
	v_cndmask_b32_e64 v36, v35, v86, s[6:7]
	v_add_f32_e32 v35, v37, v83
	ds_read2_b32 v[82:83], v121 offset0:105 offset1:106
	v_cndmask_b32_e64 v35, v35, v86, s[6:7]
	v_max3_f32 v32, v32, v36, v35
	s_waitcnt lgkmcnt(0)
	v_add_f32_e32 v37, v38, v82
	v_add_f32_e32 v38, v40, v84
	v_cndmask_b32_e64 v82, v37, v86, s[6:7]
	v_add_f32_e32 v37, v39, v83
	v_cndmask_b32_e64 v39, v38, v86, s[6:7]
	v_add_f32_e32 v38, v41, v85
	ds_read2_b32 v[84:85], v121 offset0:113 offset1:114
	v_cndmask_b32_e64 v37, v37, v86, s[6:7]
	v_max3_f32 v32, v32, v82, v37
	v_cndmask_b32_e64 v38, v38, v86, s[6:7]
	v_max3_f32 v32, v32, v39, v38
	s_waitcnt lgkmcnt(0)
	v_add_f32_e32 v40, v42, v84
	v_cndmask_b32_e64 v41, v40, v86, s[6:7]
	v_add_f32_e32 v40, v43, v85
	ds_read2_b32 v[84:85], v121 offset0:119 offset1:120
	v_cndmask_b32_e64 v40, v40, v86, s[6:7]
	v_max3_f32 v32, v32, v41, v40
	s_waitcnt lgkmcnt(0)
	v_add_f32_e32 v42, v44, v84
	v_cndmask_b32_e64 v43, v42, v86, s[6:7]
	v_add_f32_e32 v42, v45, v85
	ds_read2_b32 v[44:45], v121 offset0:121 offset1:122
	ds_read2_b32 v[84:85], v121 offset0:127 offset1:128
	v_cndmask_b32_e64 v42, v42, v86, s[6:7]
	v_max3_f32 v32, v32, v43, v42
	s_waitcnt lgkmcnt(1)
	v_add_f32_e32 v44, v46, v44
	v_cndmask_b32_e64 v46, v44, v86, s[6:7]
	v_add_f32_e32 v44, v47, v45
	s_waitcnt lgkmcnt(0)
	v_add_f32_e32 v45, v16, v84
	v_add_f32_e32 v16, v17, v85
	ds_read2_b32 v[84:85], v121 offset0:129 offset1:130
	v_cndmask_b32_e64 v44, v44, v86, s[6:7]
	v_max3_f32 v32, v32, v46, v44
	v_max3_f32 v32, v32, v45, v16
	s_waitcnt lgkmcnt(0)
	v_add_f32_e32 v18, v18, v84
	v_add_f32_e32 v17, v19, v85
	ds_read2_b32 v[84:85], v121 offset0:135 offset1:136
	v_max3_f32 v32, v32, v18, v17
	s_waitcnt lgkmcnt(0)
	v_add_f32_e32 v20, v20, v84
	v_add_f32_e32 v19, v21, v85
	ds_read2_b32 v[84:85], v121 offset0:137 offset1:138
	v_max3_f32 v32, v32, v20, v19
	s_waitcnt lgkmcnt(0)
	v_add_f32_e32 v22, v22, v84
	v_add_f32_e32 v21, v23, v85
	ds_read2_b32 v[84:85], v121 offset0:143 offset1:144
	v_max3_f32 v32, v32, v22, v21
	s_waitcnt lgkmcnt(0)
	v_add_f32_e32 v24, v24, v84
	v_add_f32_e32 v23, v25, v85
	ds_read2_b32 v[84:85], v121 offset0:145 offset1:146
	v_max3_f32 v32, v32, v24, v23
	s_waitcnt lgkmcnt(0)
	v_add_f32_e32 v26, v26, v84
	v_add_f32_e32 v25, v27, v85
	ds_read2_b32 v[84:85], v121 offset0:151 offset1:152
	v_max3_f32 v32, v32, v26, v25
	s_waitcnt lgkmcnt(0)
	v_add_f32_e32 v28, v28, v84
	v_add_f32_e32 v27, v29, v85
	ds_read2_b32 v[84:85], v121 offset0:153 offset1:154
	v_max3_f32 v32, v32, v28, v27
	s_waitcnt lgkmcnt(0)
	v_add_f32_e32 v30, v30, v84
	v_add_f32_e32 v29, v31, v85
	ds_read2_b32 v[84:85], v121 offset0:159 offset1:160
	v_max3_f32 v32, v32, v30, v29
	s_waitcnt lgkmcnt(0)
	v_add_f32_e32 v47, v0, v84
	v_add_f32_e32 v31, v1, v85
	ds_read2_b32 v[0:1], v121 offset0:161 offset1:162
	v_max3_f32 v32, v32, v47, v31
	s_waitcnt lgkmcnt(0)
	v_add_f32_e32 v161, v2, v0
	v_add_f32_e32 v160, v3, v1
	ds_read2_b32 v[0:1], v121 offset0:167 offset1:168
	v_max3_f32 v2, v32, v161, v160
	s_waitcnt lgkmcnt(0)
	v_add_f32_e32 v163, v4, v0
	v_add_f32_e32 v162, v5, v1
	ds_read2_b32 v[0:1], v121 offset0:169 offset1:170
	v_max3_f32 v2, v2, v163, v162
	s_waitcnt lgkmcnt(0)
	v_add_f32_e32 v165, v6, v0
	v_add_f32_e32 v164, v7, v1
	ds_read2_b32 v[0:1], v121 offset0:175 offset1:176
	v_max3_f32 v2, v2, v165, v164
	s_waitcnt lgkmcnt(0)
	v_add_f32_e32 v166, v8, v0
	v_add_f32_e32 v8, v9, v1
	ds_read2_b32 v[0:1], v121 offset0:177 offset1:178
	v_max3_f32 v2, v2, v166, v8
	s_waitcnt lgkmcnt(0)
	v_add_f32_e32 v10, v10, v0
	v_add_f32_e32 v9, v11, v1
	ds_read2_b32 v[0:1], v121 offset0:183 offset1:184
	v_max3_f32 v2, v2, v10, v9
	s_waitcnt lgkmcnt(0)
	v_add_f32_e32 v12, v12, v0
	v_add_f32_e32 v11, v13, v1
	ds_read2_b32 v[0:1], v121 offset0:185 offset1:186
	v_max3_f32 v2, v2, v12, v11
	s_waitcnt lgkmcnt(0)
; #define LAS __attribute__((address_space(3)))
; __device__ __forceinline__ float sum_x32(float v) { const unsigned u = __builtin_bit_cast(unsigned, v); auto rr = __builtin_amdgcn_permlane32_swap(u, u, false, false); return __builtin_bit_cast(float, (unsigned)rr[0]) + __builtin_bit_cast(float, (unsigned)rr[1]); }
; __device__ __forceinline__ float max_x32(float v) { const unsigned u = __builtin_bit_cast(unsigned, v); auto rr = __builtin_amdgcn_permlane32_swap(u, u, false, false); return fmaxf(__builtin_bit_cast(float, (unsigned)rr[0]), __builtin_bit_cast(float, (unsigned)rr[1])); }
; __device__ __forceinline__ unsigned cvt_pk_bf16(float lo, float hi) { unsigned r; asm volatile("v_cvt_pk_bf16_f32 %0, %1, %2" : "=v"(r) : "v"(lo), "v"(hi)); return r; }
; __device__ __forceinline__ void attn_phase(LAS unsigned char* lds, const bf16* U, bf16* YA, const float* sinks, const float* rel_bias, int G, int c, int wbase, int y8) {
;     ...
;             mx = max_x32(mx);
;             float l = 0.f;
; #pragma unroll
;             for (int jt = 0; jt < 5; ++jt)
; #pragma unroll
;                 for (int r = 0; r < 16; ++r) { const float e = __builtin_amdgcn_exp2f(p[jt][r] - mx); p[jt][r] = e; l += e; }
;             l = sum_x32(l); l += __builtin_amdgcn_exp2f(sink2 - mx);
;             f32x16 o[2]; o[0] = (f32x16){}; o[1] = (f32x16){};
;             const LAS unsigned char* vb = lds + VIMG + ((lane >> 4) & 1) * 32 + (lane & 3) * 8 + (4 * hi + ((lane & 15) >> 2)) * 64;
; #pragma unroll
;             for (int jt = 0; jt < 5; ++jt)
; #pragma unroll
;                 for (int s = 0; s < 2; ++s) { u32x4 w; w.x = cvt_pk_bf16(p[jt][8 * s], p[jt][8 * s + 1]); w.y = cvt_pk_bf16(p[jt][8 * s + 2], p[jt][8 * s + 3]); w.z = cvt_pk_bf16(p[jt][8 * s + 4], p[jt][8 * s + 5]); w.w = cvt_pk_bf16(p[jt][8 * s + 6], p[jt][8 * s + 7]);
;                     const bf16x8 pa = __builtin_bit_cast(bf16x8, w);
; #pragma unroll
;                     for (int d0 = 0; d0 < 2; ++d0) { const LAS unsigned char* vp = vb + d0 * 16384 + (32 * (kt0 + jt) + 16 * s) * 64; const s16x4 lo = vtr(vp), hv = vtr(vp + 8 * 64);
;                         const bf16x8 vf = (bf16x8){lo[0], lo[1], lo[2], lo[3], hv[0], hv[1], hv[2], hv[3]};
;                         o[d0] = __builtin_amdgcn_mfma_f32_32x32x16_bf16(pa, vf, o[d0], 0, 0, 0); } }
	v_add_f32_e32 v14, v14, v0
	v_add_f32_e32 v13, v15, v1
	v_max3_f32 v0, v2, v14, v13
	v_mov_b32_e32 v1, v0
	s_nop 1
	v_permlane32_swap_b32_e32 v0, v1
	v_max_f32_e32 v1, v1, v1
	v_max_f32_e32 v0, v0, v0
	v_max_f32_e32 v32, v0, v1
	v_sub_f32_e32 v0, v80, v32
	v_exp_f32_e32 v0, v0
	v_sub_f32_e32 v1, v64, v32
	v_exp_f32_e32 v1, v1
	v_sub_f32_e32 v64, v71, v32
	v_add_f32_e32 v2, 0, v0
	v_exp_f32_e32 v64, v64
	v_add_f32_e32 v3, v1, v2
	v_sub_f32_e32 v2, v66, v32
	v_exp_f32_e32 v2, v2
	v_sub_f32_e32 v48, v48, v32
	v_sub_f32_e32 v33, v33, v32
	v_sub_f32_e32 v16, v16, v32
	v_add_f32_e32 v4, v2, v3
	v_sub_f32_e32 v3, v65, v32
	v_exp_f32_e32 v3, v3
	v_sub_f32_e32 v65, v69, v32
	v_exp_f32_e32 v66, v65
	v_sub_f32_e32 v65, v73, v32
	v_add_f32_e32 v5, v3, v4
	v_sub_f32_e32 v4, v68, v32
	v_exp_f32_e32 v4, v4
	v_exp_f32_e32 v68, v65
	v_sub_f32_e32 v65, v72, v32
	v_exp_f32_e32 v72, v65
	v_add_f32_e32 v6, v4, v5
	v_sub_f32_e32 v5, v67, v32
	v_exp_f32_e32 v5, v5
	v_sub_f32_e32 v65, v75, v32
	v_exp_f32_e32 v75, v65
	v_sub_f32_e32 v65, v74, v32
	v_add_f32_e32 v7, v5, v6
	v_sub_f32_e32 v6, v81, v32
	v_exp_f32_e32 v6, v6
	v_exp_f32_e32 v81, v65
	v_sub_f32_e32 v65, v78, v32
	v_exp_f32_e32 v86, v65
	v_add_f32_e32 v15, v6, v7
	v_sub_f32_e32 v7, v70, v32
	v_exp_f32_e32 v7, v7
	v_sub_f32_e32 v65, v76, v32
	v_exp_f32_e32 v107, v65
	v_sub_f32_e32 v65, v77, v32
	v_add_f32_e32 v15, v7, v15
	v_add_f32_e32 v15, v64, v15
	v_add_f32_e32 v15, v66, v15
	v_add_f32_e32 v15, v68, v15
	v_add_f32_e32 v15, v72, v15
	v_add_f32_e32 v15, v75, v15
	v_exp_f32_e32 v65, v65
	v_add_f32_e32 v15, v81, v15
	v_exp_f32_e32 v67, v48
	v_sub_f32_e32 v48, v50, v32
	v_add_f32_e32 v15, v86, v15
	v_exp_f32_e32 v70, v48
	v_sub_f32_e32 v48, v49, v32
	v_add_f32_e32 v15, v107, v15
	v_exp_f32_e32 v76, v48
	v_sub_f32_e32 v48, v52, v32
	v_add_f32_e32 v15, v65, v15
	v_exp_f32_e32 v80, v48
	v_sub_f32_e32 v48, v51, v32
	v_add_f32_e32 v15, v67, v15
	v_exp_f32_e32 v85, v48
	v_sub_f32_e32 v48, v79, v32
	v_add_f32_e32 v15, v70, v15
	v_exp_f32_e32 v91, v48
	v_sub_f32_e32 v48, v54, v32
	v_add_f32_e32 v15, v76, v15
	v_exp_f32_e32 v155, v48
	v_sub_f32_e32 v48, v55, v32
	v_add_f32_e32 v15, v80, v15
	v_exp_f32_e32 v54, v48
	v_sub_f32_e32 v48, v53, v32
	v_add_f32_e32 v15, v85, v15
	v_exp_f32_e32 v69, v48
	v_sub_f32_e32 v48, v57, v32
	v_add_f32_e32 v15, v91, v15
	v_exp_f32_e32 v71, v48
	v_sub_f32_e32 v48, v56, v32
	v_add_f32_e32 v15, v155, v15
	v_exp_f32_e32 v79, v48
	v_sub_f32_e32 v48, v59, v32
	v_add_f32_e32 v15, v54, v15
	v_exp_f32_e32 v83, v48
	v_sub_f32_e32 v48, v58, v32
	v_add_f32_e32 v15, v69, v15
	v_exp_f32_e32 v89, v48
	v_sub_f32_e32 v48, v62, v32
	v_add_f32_e32 v15, v71, v15
	v_exp_f32_e32 v105, v48
	v_sub_f32_e32 v48, v60, v32
	v_add_f32_e32 v15, v79, v15
	v_exp_f32_e32 v157, v48
	v_sub_f32_e32 v48, v61, v32
	v_add_f32_e32 v15, v83, v15
	v_exp_f32_e32 v58, v48
	v_add_f32_e32 v15, v89, v15
	v_exp_f32_e32 v62, v33
	v_sub_f32_e32 v33, v63, v32
	v_add_f32_e32 v15, v105, v15
	v_exp_f32_e32 v74, v33
	v_sub_f32_e32 v33, v34, v32
	v_add_f32_e32 v15, v157, v15
	v_exp_f32_e32 v84, v33
	v_sub_f32_e32 v33, v36, v32
	v_add_f32_e32 v15, v58, v15
	v_exp_f32_e32 v87, v33
	v_sub_f32_e32 v33, v35, v32
	v_add_f32_e32 v15, v62, v15
	v_exp_f32_e32 v94, v33
	v_sub_f32_e32 v33, v82, v32
	v_add_f32_e32 v15, v74, v15
	v_exp_f32_e32 v154, v33
	v_sub_f32_e32 v33, v37, v32
	v_add_f32_e32 v15, v84, v15
	v_exp_f32_e32 v158, v33
	v_sub_f32_e32 v33, v39, v32
	v_add_f32_e32 v15, v87, v15
	v_exp_f32_e32 v61, v33
	v_sub_f32_e32 v33, v38, v32
	v_add_f32_e32 v15, v94, v15
	v_exp_f32_e32 v73, v33
	v_sub_f32_e32 v33, v41, v32
	v_add_f32_e32 v15, v154, v15
	v_exp_f32_e32 v78, v33
	v_sub_f32_e32 v33, v40, v32
	v_add_f32_e32 v15, v158, v15
	v_exp_f32_e32 v88, v33
	v_sub_f32_e32 v33, v43, v32
	v_add_f32_e32 v15, v61, v15
	v_exp_f32_e32 v93, v33
	v_sub_f32_e32 v33, v42, v32
	v_add_f32_e32 v15, v73, v15
	v_exp_f32_e32 v153, v33
	v_sub_f32_e32 v33, v46, v32
	v_add_f32_e32 v15, v78, v15
	v_exp_f32_e32 v156, v33
	v_sub_f32_e32 v33, v44, v32
	v_add_f32_e32 v15, v88, v15
	v_exp_f32_e32 v159, v33
	v_sub_f32_e32 v33, v45, v32
	v_add_f32_e32 v15, v93, v15
	v_exp_f32_e32 v63, v33
	v_add_f32_e32 v15, v153, v15
	v_exp_f32_e32 v77, v16
	v_sub_f32_e32 v16, v18, v32
	v_add_f32_e32 v15, v156, v15
	v_exp_f32_e32 v82, v16
	v_sub_f32_e32 v16, v17, v32
	v_add_f32_e32 v15, v159, v15
	v_exp_f32_e32 v90, v16
	v_sub_f32_e32 v16, v20, v32
	v_add_f32_e32 v15, v63, v15
	v_exp_f32_e32 v92, v16
	v_sub_f32_e32 v16, v19, v32
	v_add_f32_e32 v15, v77, v15
	v_exp_f32_e32 v95, v16
	v_sub_f32_e32 v16, v22, v32
	v_add_f32_e32 v15, v82, v15
	v_exp_f32_e32 v106, v16
	v_sub_f32_e32 v16, v21, v32
	v_add_f32_e32 v15, v90, v15
	v_exp_f32_e32 v152, v16
	v_sub_f32_e32 v16, v24, v32
	v_add_f32_e32 v15, v92, v15
	v_exp_f32_e32 v51, v16
	v_sub_f32_e32 v16, v23, v32
	v_add_f32_e32 v15, v95, v15
	v_exp_f32_e32 v52, v16
	v_sub_f32_e32 v16, v26, v32
	v_add_f32_e32 v15, v106, v15
	v_exp_f32_e32 v53, v16
	v_sub_f32_e32 v16, v25, v32
	v_add_f32_e32 v15, v152, v15
	v_exp_f32_e32 v55, v16
	v_sub_f32_e32 v16, v28, v32
	v_add_f32_e32 v15, v51, v15
	v_exp_f32_e32 v56, v16
	v_sub_f32_e32 v16, v27, v32
	v_add_f32_e32 v15, v52, v15
	v_exp_f32_e32 v57, v16
	v_sub_f32_e32 v16, v30, v32
	v_add_f32_e32 v15, v53, v15
	v_exp_f32_e32 v59, v16
	v_sub_f32_e32 v16, v29, v32
	v_add_f32_e32 v15, v55, v15
	v_exp_f32_e32 v60, v16
	v_sub_f32_e32 v16, v47, v32
	v_add_f32_e32 v15, v56, v15
	v_exp_f32_e32 v43, v16
	v_sub_f32_e32 v16, v31, v32
	v_add_f32_e32 v15, v57, v15
	v_exp_f32_e32 v44, v16
	v_sub_f32_e32 v16, v161, v32
	v_add_f32_e32 v15, v59, v15
	v_exp_f32_e32 v45, v16
	v_sub_f32_e32 v16, v160, v32
	v_add_f32_e32 v15, v60, v15
	v_exp_f32_e32 v46, v16
	v_sub_f32_e32 v16, v163, v32
	v_add_f32_e32 v15, v43, v15
	v_exp_f32_e32 v47, v16
	v_sub_f32_e32 v16, v162, v32
	v_add_f32_e32 v15, v44, v15
	v_exp_f32_e32 v48, v16
	v_sub_f32_e32 v16, v165, v32
	v_add_f32_e32 v15, v45, v15
	v_exp_f32_e32 v49, v16
	v_sub_f32_e32 v16, v164, v32
	v_add_f32_e32 v15, v46, v15
	v_exp_f32_e32 v50, v16
	v_sub_f32_e32 v16, v166, v32
	v_add_f32_e32 v15, v47, v15
	v_exp_f32_e32 v35, v16
	v_sub_f32_e32 v8, v8, v32
	v_add_f32_e32 v15, v48, v15
	v_exp_f32_e32 v36, v8
	v_sub_f32_e32 v10, v10, v32
	v_add_f32_e32 v15, v49, v15
	v_exp_f32_e32 v37, v10
	v_sub_f32_e32 v9, v9, v32
	v_add_f32_e32 v15, v50, v15
	v_exp_f32_e32 v38, v9
	v_sub_f32_e32 v9, v12, v32
	v_add_f32_e32 v15, v35, v15
	v_exp_f32_e32 v39, v9
	v_sub_f32_e32 v9, v11, v32
	v_add_f32_e32 v8, v36, v15
	v_exp_f32_e32 v40, v9
	v_sub_f32_e32 v9, v14, v32
	v_add_f32_e32 v8, v37, v8
	v_exp_f32_e32 v41, v9
	v_sub_f32_e32 v9, v13, v32
	v_cvt_pk_bf16_f32 v16, v0, v1
	v_cvt_pk_bf16_f32 v17, v2, v3
	v_cvt_pk_bf16_f32 v18, v4, v5
	v_cvt_pk_bf16_f32 v19, v6, v7
	ds_read_b64_tr_b16 v[0:1], v101 offset:32768
	ds_read_b64_tr_b16 v[2:3], v101 offset:33280
	v_add_f32_e32 v8, v38, v8
	v_exp_f32_e32 v42, v9
	v_add_f32_e32 v8, v39, v8
	v_add_f32_e32 v8, v40, v8
	v_add_f32_e32 v8, v41, v8
	v_add_f32_e32 v33, v42, v8
	s_waitcnt lgkmcnt(0)
; #define LAS __attribute__((address_space(3)))
; __device__ __forceinline__ float sum_x32(float v) { const unsigned u = __builtin_bit_cast(unsigned, v); auto rr = __builtin_amdgcn_permlane32_swap(u, u, false, false); return __builtin_bit_cast(float, (unsigned)rr[0]) + __builtin_bit_cast(float, (unsigned)rr[1]); }
; __device__ __forceinline__ unsigned cvt_pk_bf16(float lo, float hi) { unsigned r; asm volatile("v_cvt_pk_bf16_f32 %0, %1, %2" : "=v"(r) : "v"(lo), "v"(hi)); return r; }
; __device__ __forceinline__ s16x4 vtr(const LAS unsigned char* p) { return __builtin_bit_cast(s16x4, __builtin_amdgcn_ds_read_tr16_b64_v4i16((LAS s16x4*)p)); }
; __device__ __forceinline__ void attn_phase(LAS unsigned char* lds, const bf16* U, bf16* YA, const float* sinks, const float* rel_bias, int G, int c, int wbase, int y8) {
;     ...
;             l = sum_x32(l); l += __builtin_amdgcn_exp2f(sink2 - mx);
;             f32x16 o[2]; o[0] = (f32x16){}; o[1] = (f32x16){};
;             const LAS unsigned char* vb = lds + VIMG + ((lane >> 4) & 1) * 32 + (lane & 3) * 8 + (4 * hi + ((lane & 15) >> 2)) * 64;
; #pragma unroll
;             for (int jt = 0; jt < 5; ++jt)
; #pragma unroll
;                 for (int s = 0; s < 2; ++s) { u32x4 w; w.x = cvt_pk_bf16(p[jt][8 * s], p[jt][8 * s + 1]); w.y = cvt_pk_bf16(p[jt][8 * s + 2], p[jt][8 * s + 3]); w.z = cvt_pk_bf16(p[jt][8 * s + 4], p[jt][8 * s + 5]); w.w = cvt_pk_bf16(p[jt][8 * s + 6], p[jt][8 * s + 7]);
;                     const bf16x8 pa = __builtin_bit_cast(bf16x8, w);
; #pragma unroll
;                     for (int d0 = 0; d0 < 2; ++d0) { const LAS unsigned char* vp = vb + d0 * 16384 + (32 * (kt0 + jt) + 16 * s) * 64; const s16x4 lo = vtr(vp), hv = vtr(vp + 8 * 64);
;                         const bf16x8 vf = (bf16x8){lo[0], lo[1], lo[2], lo[3], hv[0], hv[1], hv[2], hv[3]};
;                         o[d0] = __builtin_amdgcn_mfma_f32_32x32x16_bf16(pa, vf, o[d0], 0, 0, 0); } }
;             if (hi == 0) lscr[r32] = l;
	v_mfma_f32_32x32x16_bf16 v[0:15], v[16:19], v[0:3], 0
	ds_read_b64_tr_b16 v[20:21], v101 offset:49152
	ds_read_b64_tr_b16 v[22:23], v101 offset:49664
	v_cvt_pk_bf16_f32 v160, v64, v66
	v_cvt_pk_bf16_f32 v161, v68, v72
	v_cvt_pk_bf16_f32 v162, v75, v81
	v_cvt_pk_bf16_f32 v163, v86, v107
	ds_read_b64_tr_b16 v[164:165], v101 offset:33792
	ds_read_b64_tr_b16 v[166:167], v101 offset:34304
	v_mov_b32_e32 v34, v33
	s_waitcnt lgkmcnt(2)
	v_mfma_f32_32x32x16_bf16 v[16:31], v[16:19], v[20:23], 0
	v_permlane32_swap_b32_e32 v33, v34
	s_waitcnt lgkmcnt(0)
	v_mfma_f32_32x32x16_bf16 v[0:15], v[160:163], v[164:167], v[0:15]
	ds_read_b64_tr_b16 v[164:165], v101 offset:50176
	ds_read_b64_tr_b16 v[166:167], v101 offset:50688
	v_cvt_pk_bf16_f32 v64, v65, v67
	v_cvt_pk_bf16_f32 v65, v70, v76
	v_cvt_pk_bf16_f32 v66, v80, v85
	v_cvt_pk_bf16_f32 v67, v91, v155
	s_waitcnt lgkmcnt(0)
	v_mfma_f32_32x32x16_bf16 v[16:31], v[160:163], v[164:167], v[16:31]
	ds_read_b64_tr_b16 v[160:161], v102 offset:32768
	ds_read_b64_tr_b16 v[162:163], v102 offset:33280
	s_waitcnt lgkmcnt(0)
	v_mfma_f32_32x32x16_bf16 v[0:15], v[64:67], v[160:163], v[0:15]
	ds_read_b64_tr_b16 v[160:161], v102 offset:49152
	ds_read_b64_tr_b16 v[162:163], v102 offset:49664
	s_waitcnt lgkmcnt(0)
	v_mfma_f32_32x32x16_bf16 v[16:31], v[64:67], v[160:163], v[16:31]
	v_cvt_pk_bf16_f32 v64, v54, v69
	v_cvt_pk_bf16_f32 v65, v71, v79
	v_cvt_pk_bf16_f32 v66, v83, v89
	v_cvt_pk_bf16_f32 v67, v105, v157
	ds_read_b64_tr_b16 v[68:69], v102 offset:33792
	ds_read_b64_tr_b16 v[70:71], v102 offset:34304
	s_waitcnt lgkmcnt(0)
	v_mfma_f32_32x32x16_bf16 v[0:15], v[64:67], v[68:71], v[0:15]
	ds_read_b64_tr_b16 v[68:69], v102 offset:50176
	ds_read_b64_tr_b16 v[70:71], v102 offset:50688
	s_waitcnt lgkmcnt(0)
	v_mfma_f32_32x32x16_bf16 v[16:31], v[64:67], v[68:71], v[16:31]
	v_cvt_pk_bf16_f32 v64, v58, v62
	v_cvt_pk_bf16_f32 v65, v74, v84
	v_cvt_pk_bf16_f32 v66, v87, v94
	v_cvt_pk_bf16_f32 v67, v154, v158
	ds_read_b64_tr_b16 v[68:69], v103 offset:32768
	ds_read_b64_tr_b16 v[70:71], v103 offset:33280
	s_waitcnt lgkmcnt(0)
	v_mfma_f32_32x32x16_bf16 v[0:15], v[64:67], v[68:71], v[0:15]
	ds_read_b64_tr_b16 v[68:69], v103 offset:49152
	ds_read_b64_tr_b16 v[70:71], v103 offset:49664
	s_waitcnt lgkmcnt(0)
	v_mfma_f32_32x32x16_bf16 v[16:31], v[64:67], v[68:71], v[16:31]
	v_cvt_pk_bf16_f32 v64, v61, v73
	v_cvt_pk_bf16_f32 v65, v78, v88
	v_cvt_pk_bf16_f32 v66, v93, v153
	v_cvt_pk_bf16_f32 v67, v156, v159
	ds_read_b64_tr_b16 v[68:69], v103 offset:33792
	ds_read_b64_tr_b16 v[70:71], v103 offset:34304
	s_waitcnt lgkmcnt(0)
	v_mfma_f32_32x32x16_bf16 v[0:15], v[64:67], v[68:71], v[0:15]
	ds_read_b64_tr_b16 v[68:69], v103 offset:50176
	ds_read_b64_tr_b16 v[70:71], v103 offset:50688
	v_cvt_pk_bf16_f32 v62, v63, v77
	v_cvt_pk_bf16_f32 v63, v82, v90
	s_waitcnt lgkmcnt(0)
	v_mfma_f32_32x32x16_bf16 v[16:31], v[64:67], v[68:71], v[16:31]
	v_cvt_pk_bf16_f32 v64, v92, v95
	v_cvt_pk_bf16_f32 v65, v106, v152
	ds_read_b64_tr_b16 v[66:67], v104 offset:32768
	ds_read_b64_tr_b16 v[68:69], v104 offset:33280
	s_waitcnt lgkmcnt(0)
	v_mfma_f32_32x32x16_bf16 v[0:15], v[62:65], v[66:69], v[0:15]
	ds_read_b64_tr_b16 v[66:67], v104 offset:49152
	ds_read_b64_tr_b16 v[68:69], v104 offset:49664
	v_cvt_pk_bf16_f32 v52, v51, v52
	v_cvt_pk_bf16_f32 v53, v53, v55
	v_cvt_pk_bf16_f32 v54, v56, v57
	v_cvt_pk_bf16_f32 v55, v59, v60
	ds_read_b64_tr_b16 v[56:57], v104 offset:33792
	ds_read_b64_tr_b16 v[58:59], v104 offset:34304
	s_waitcnt lgkmcnt(2)
	v_mfma_f32_32x32x16_bf16 v[16:31], v[62:65], v[66:69], v[16:31]
	s_waitcnt lgkmcnt(0)
	v_mfma_f32_32x32x16_bf16 v[0:15], v[52:55], v[56:59], v[0:15]
	ds_read_b64_tr_b16 v[56:57], v104 offset:50176
	ds_read_b64_tr_b16 v[58:59], v104 offset:50688
	v_cvt_pk_bf16_f32 v44, v43, v44
	v_cvt_pk_bf16_f32 v45, v45, v46
	v_cvt_pk_bf16_f32 v46, v47, v48
	v_cvt_pk_bf16_f32 v47, v49, v50
	s_waitcnt lgkmcnt(0)
	v_mfma_f32_32x32x16_bf16 v[16:31], v[52:55], v[56:59], v[16:31]
	v_add_u32_e32 v52, s79, v125
	ds_read_b64_tr_b16 v[48:49], v52 offset:32768
	ds_read_b64_tr_b16 v[50:51], v52 offset:33280
	s_waitcnt lgkmcnt(0)
	v_mfma_f32_32x32x16_bf16 v[0:15], v[44:47], v[48:51], v[0:15]
	ds_read_b64_tr_b16 v[48:49], v52 offset:49152
	ds_read_b64_tr_b16 v[50:51], v52 offset:49664
	v_cvt_pk_bf16_f32 v36, v35, v36
	v_cvt_pk_bf16_f32 v37, v37, v38
	v_cvt_pk_bf16_f32 v38, v39, v40
	v_cvt_pk_bf16_f32 v39, v41, v42
	ds_read_b64_tr_b16 v[40:41], v52 offset:33792
	ds_read_b64_tr_b16 v[42:43], v52 offset:34304
	s_waitcnt lgkmcnt(2)
	v_mfma_f32_32x32x16_bf16 v[16:31], v[44:47], v[48:51], v[16:31]
	s_waitcnt lgkmcnt(0)
	v_mfma_f32_32x32x16_bf16 v[0:15], v[36:39], v[40:43], v[0:15]
	ds_read_b64_tr_b16 v[40:41], v52 offset:50176
	ds_read_b64_tr_b16 v[42:43], v52 offset:50688
	s_waitcnt lgkmcnt(0)
	v_mfma_f32_32x32x16_bf16 v[16:31], v[36:39], v[40:43], v[16:31]
	s_and_saveexec_b64 s[4:5], s[2:3]
	s_cbranch_execz .LBB0_570
	v_sub_f32_e32 v32, v151, v32
	v_exp_f32_e32 v32, v32
	v_add_f32_e32 v33, v33, v34
	v_add_f32_e32 v32, v33, v32
	ds_write_b32 v126, v32

; #define LAS __attribute__((address_space(3)))
; __device__ __forceinline__ void lru_scan(LAS unsigned char* lds, const bf16* U, bf16* HR, bf16* PQ, float* AGG, const bf16* Wt, const float* conv_w, const float* conv_b,
;                                          const float* b_rg, const float* b_ig, const float* lam, int G, int c, int wbase) {
;     ...
;             for (int ct = 0; ct < 2; ++ct) {
;                 f32x16 R = {}, I = {}, X = {};
;                 int zoff; asm volatile("v_mov_b32 %0, 0" : "=v"(zoff)); const LAS unsigned char* Wp = lds + WL_OFF + zoff;
;                 bf16x8 wr[4], wi[4];
; #pragma unroll
;                 for (int ks = 0; ks < 4; ++ks) { const int o = (32 * ct + r32) * WL_ROW + (16 * ks + 8 * hi) * 2; wr[ks] = *(const LAS bf16x8*)(Wp + o); wi[ks] = *(const LAS bf16x8*)(Wp + 64 * WL_ROW + o); }
; #pragma unroll
;                 for (int ks = 0; ks < 4; ++ks) { bf16x8 idf;
; #pragma unroll
;                     for (int j = 0; j < 8; ++j) idf[j] = (16 * ks + 8 * hi + j == 32 * ct + r32) ? (short)0x3F80 : (short)0;
;                     R = __builtin_amdgcn_mfma_f32_32x32x16_bf16(af[ks], wr[ks], R, 0, 0, 0); I = __builtin_amdgcn_mfma_f32_32x32x16_bf16(af[ks], wi[ks], I, 0, 0, 0);
;                     X = __builtin_amdgcn_mfma_f32_32x32x16_bf16(af[ks], idf, X, 0, 0, 0); }
;                 float P[16], H[16];
; #pragma unroll
;                 for (int r = 0; r < 16; ++r) { const float er = __builtin_amdgcn_exp2f(R[r] * -LOG2E + brg[ct]), ei = __builtin_amdgcn_exp2f(I[r] * -LOG2E + big[ct]);
;                     const float e1 = 1.f + er, e2 = 1.f + ei, qq = __builtin_amdgcn_rcpf(e1 * e2), rr = qq * e2, ii = qq * e1;
;                     const float a = __builtin_amdgcn_exp2f(rr * sp8[ct]);
;                     P[r] = a; H[r] = __builtin_amdgcn_sqrtf(fmaxf(1.f - a * a, 0.f)) * (ii * X[r]); }
.LBB0_604:
	v_mov_b32 v0, 0
	s_mov_b32 s42, s40
	v_add_u32_e32 v12, v198, v0
	ds_read_b128 v[0:3], v12
	ds_read_b128 v[4:7], v12 offset:32
	s_mov_b32 s43, s40
	s_waitcnt lgkmcnt(1)
	v_mfma_f32_32x32x16_bf16 v[14:29], v[124:127], v[0:3], 0
	ds_read_b128 v[0:3], v12 offset:9216
	ds_read_b128 v[8:11], v12 offset:9248
	s_mov_b32 s41, s40
	v_mov_b64_e32 v[142:143], s[42:43]
	v_mov_b64_e32 v[140:141], s[40:41]
	s_add_i32 s34, s34, 32
	s_mov_b64 s[4:5], 0x58000
	v_lshl_add_u64 v[154:155], v[154:155], 0, s[4:5]
	s_waitcnt lgkmcnt(1)
	v_mfma_f32_32x32x16_bf16 v[30:45], v[124:127], v[0:3], 0
	s_cmpk_eq_i32 s34, 0x80
	v_mfma_f32_32x32x16_bf16 v[14:29], v[128:131], v[4:7], v[14:29]
	ds_read_b128 v[0:3], v12 offset:64
	ds_read_b128 v[4:7], v12 offset:96
	s_waitcnt lgkmcnt(2)
	v_mfma_f32_32x32x16_bf16 v[30:45], v[128:131], v[8:11], v[30:45]
	s_waitcnt lgkmcnt(1)
	v_mfma_f32_32x32x16_bf16 v[14:29], v[132:135], v[0:3], v[14:29]
	ds_read_b128 v[0:3], v12 offset:9280
	ds_read_b128 v[8:11], v12 offset:9312
	s_waitcnt lgkmcnt(1)
	v_mfma_f32_32x32x16_bf16 v[30:45], v[132:135], v[0:3], v[30:45]
	v_mfma_f32_32x32x16_bf16 v[14:29], v[136:139], v[4:7], v[14:29]
	s_waitcnt lgkmcnt(0)
	v_mfma_f32_32x32x16_bf16 v[30:45], v[136:139], v[8:11], v[30:45]
	s_nop 9
	v_fmamk_f32 v0, v14, 0xbfb8aa3b, v203
	v_exp_f32_e32 v0, v0
	v_fmamk_f32 v18, v18, 0xbfb8aa3b, v203
	v_fmamk_f32 v21, v21, 0xbfb8aa3b, v203
	v_fmamk_f32 v22, v22, 0xbfb8aa3b, v203
	v_fmamk_f32 v1, v30, 0xbfb8aa3b, v204
	v_exp_f32_e32 v1, v1
	v_fmamk_f32 v3, v31, 0xbfb8aa3b, v204
	v_exp_f32_e32 v3, v3
	v_pk_add_f32 v[0:1], v[0:1], 1.0 op_sel_hi:[1,0]
	s_nop 0
	v_mul_f32_e32 v2, v0, v1
	v_rcp_f32_e32 v4, v2
	v_fmamk_f32 v2, v15, 0xbfb8aa3b, v203
	v_exp_f32_e32 v2, v2
	v_mul_f32_e32 v1, v1, v4
	v_mul_f32_e32 v1, v153, v1
	v_pk_add_f32 v[172:173], v[2:3], 1.0 op_sel_hi:[1,0]
	v_exp_f32_e32 v165, v1
	v_mul_f32_e32 v1, v172, v173
	v_rcp_f32_e32 v174, v1
	v_mul_f32_e32 v166, v0, v4
	v_fmamk_f32 v1, v32, 0xbfb8aa3b, v204
	v_exp_f32_e32 v1, v1
	v_mul_f32_e32 v0, v173, v174
	v_mul_f32_e32 v0, v153, v0
	v_exp_f32_e32 v47, v0
	v_fmamk_f32 v0, v16, 0xbfb8aa3b, v203
	v_exp_f32_e32 v0, v0
	v_fma_f32 v2, -v165, v165, 1.0
	v_max_f32_e32 v2, 0, v2
	v_sqrt_f32_e32 v169, v2
	v_pk_add_f32 v[30:31], v[0:1], 1.0 op_sel_hi:[1,0]
	v_fma_f32 v2, -v47, v47, 1.0
	v_mul_f32_e32 v0, v30, v31
	v_rcp_f32_e32 v32, v0
	v_max_f32_e32 v0, 0, v2
	v_sqrt_f32_e32 v46, v0
	v_mfma_f32_32x32x16_bf16 v[0:15], v[124:127], v[48:51], 0
	v_mul_f32_e32 v16, v31, v32
	v_mul_f32_e32 v16, v153, v16
	v_exp_f32_e32 v31, v16
	v_fmamk_f32 v16, v17, 0xbfb8aa3b, v203
	v_fmamk_f32 v17, v33, 0xbfb8aa3b, v204
	v_exp_f32_e32 v16, v16
	v_exp_f32_e32 v17, v17
	v_mfma_f32_32x32x16_bf16 v[0:15], v[128:131], v[52:55], v[0:15]
	v_mul_f32_e32 v170, v30, v32
	v_fma_f32 v30, -v31, v31, 1.0
	v_add_f32_e64 v16, v16, 1.0
	v_add_f32_e64 v17, v17, 1.0
	v_max_f32_e32 v30, 0, v30
	v_mul_f32_e32 v32, v16, v17
	v_rcp_f32_e32 v173, v32
	v_exp_f32_e32 v32, v18
	v_mfma_f32_32x32x16_bf16 v[0:15], v[132:135], v[140:143], v[0:15]
	v_fmamk_f32 v18, v34, 0xbfb8aa3b, v204
	v_exp_f32_e32 v33, v18
	v_mul_f32_e32 v17, v17, v173
	v_mul_f32_e32 v17, v153, v17
	v_exp_f32_e32 v17, v17
	v_pk_add_f32 v[32:33], v[32:33], 1.0 op_sel_hi:[1,0]
	v_sqrt_f32_e32 v30, v30
	v_mfma_f32_32x32x16_bf16 v[0:15], v[136:139], v[140:143], v[0:15]
	v_mul_f32_e32 v18, v32, v33
	v_rcp_f32_e32 v18, v18
	s_nop 9
	v_mul_f32_e32 v34, v2, v170
	v_mul_f32_e32 v2, v16, v173
	v_mul_f32_e32 v176, v3, v2
	v_mul_f32_e32 v2, v33, v18
	v_mul_f32_e32 v2, v153, v2
	v_fmamk_f32 v3, v19, 0xbfb8aa3b, v203
	v_mul_f32_e32 v170, v32, v18
	v_exp_f32_e32 v2, v2
	v_exp_f32_e32 v18, v3
	v_fmamk_f32 v3, v35, 0xbfb8aa3b, v204
	v_exp_f32_e32 v19, v3
	v_fma_f32 v3, -v2, v2, 1.0
	v_max_f32_e32 v3, 0, v3
	v_sqrt_f32_e32 v193, v3
	v_pk_add_f32 v[178:179], v[18:19], 1.0 op_sel_hi:[1,0]
	v_pk_mov_b32 v[0:1], v[0:1], v[0:1] op_sel:[1,0]
	v_mul_f32_e32 v3, v178, v179
	v_rcp_f32_e32 v180, v3
	v_fmamk_f32 v3, v20, 0xbfb8aa3b, v203
	v_exp_f32_e32 v32, v3
	v_fmamk_f32 v3, v36, 0xbfb8aa3b, v204
	v_exp_f32_e32 v33, v3
	v_mul_f32_e32 v3, v179, v180
	v_mul_f32_e32 v3, v153, v3
	v_exp_f32_e32 v19, v3
	v_pk_add_f32 v[32:33], v[32:33], 1.0 op_sel_hi:[1,0]
	v_exp_f32_e32 v36, v21
	v_mul_f32_e32 v3, v32, v33
	v_rcp_f32_e32 v3, v3
	v_fmamk_f32 v21, v37, 0xbfb8aa3b, v204
	v_exp_f32_e32 v37, v21
	v_mov_b32_e32 v173, v166
	v_mul_f32_e32 v20, v33, v3
	v_mul_f32_e32 v3, v32, v3
	v_mul_f32_e32 v20, v153, v20
	v_pk_add_f32 v[32:33], v[36:37], 1.0 op_sel_hi:[1,0]
	v_exp_f32_e32 v21, v20
	v_mul_f32_e32 v20, v32, v33
	v_exp_f32_e32 v36, v22
	v_fmamk_f32 v22, v38, 0xbfb8aa3b, v204
	v_rcp_f32_e32 v35, v20
	v_exp_f32_e32 v37, v22
	v_mul_f32_e32 v38, v6, v3
	v_mov_b32_e32 v175, v1
	v_mul_f32_e32 v33, v33, v35
	v_pk_add_f32 v[36:37], v[36:37], 1.0 op_sel_hi:[1,0]
	v_mul_f32_e32 v33, v153, v33
	v_mul_f32_e32 v22, v36, v37
	v_exp_f32_e32 v33, v33
	v_mul_f32_e32 v3, v32, v35
	v_rcp_f32_e32 v35, v22
	v_mul_f32_e32 v208, v7, v3
	v_fma_f32 v6, -v33, v33, 1.0
	v_max_f32_e32 v6, 0, v6
	v_mul_f32_e32 v3, v37, v35
	v_mul_f32_e32 v3, v153, v3
	v_sqrt_f32_e32 v32, v6
	v_exp_f32_e32 v6, v3
	v_fmamk_f32 v3, v23, 0xbfb8aa3b, v203
	v_exp_f32_e32 v22, v3
	v_fmamk_f32 v3, v39, 0xbfb8aa3b, v204
	v_exp_f32_e32 v23, v3
	v_mul_f32_e32 v207, v36, v35
	v_fma_f32 v3, -v6, v6, 1.0
	v_max_f32_e32 v3, 0, v3
	v_pk_add_f32 v[210:211], v[22:23], 1.0 op_sel_hi:[1,0]
	v_sqrt_f32_e32 v216, v3
	v_mul_f32_e32 v7, v210, v211
	v_rcp_f32_e32 v212, v7
	v_fmamk_f32 v7, v24, 0xbfb8aa3b, v203
	v_exp_f32_e32 v36, v7
	v_fmamk_f32 v7, v40, 0xbfb8aa3b, v204
	v_exp_f32_e32 v37, v7
	v_mul_f32_e32 v7, v211, v212
	v_mul_f32_e32 v7, v153, v7
; __device__ __forceinline__ float get_x32(float v, int hi) { const unsigned u = __builtin_bit_cast(unsigned, v); auto rr = __builtin_amdgcn_permlane32_swap(u, u, false, false); return __builtin_bit_cast(float, hi ? (unsigned)rr[0] : (unsigned)rr[1]); }
; __device__ __forceinline__ void lru_scan(LAS unsigned char* lds, const bf16* U, bf16* HR, bf16* PQ, float* AGG, const bf16* Wt, const float* conv_w, const float* conv_b,
;                                          const float* b_rg, const float* b_ig, const float* lam, int G, int c, int wbase) {
;     ...
;                 for (int r = 0; r < 16; ++r) { const float er = __builtin_amdgcn_exp2f(R[r] * -LOG2E + brg[ct]), ei = __builtin_amdgcn_exp2f(I[r] * -LOG2E + big[ct]);
;                     const float e1 = 1.f + er, e2 = 1.f + ei, qq = __builtin_amdgcn_rcpf(e1 * e2), rr = qq * e2, ii = qq * e1;
;                     const float a = __builtin_amdgcn_exp2f(rr * sp8[ct]);
;                     P[r] = a; H[r] = __builtin_amdgcn_sqrtf(fmaxf(1.f - a * a, 0.f)) * (ii * X[r]); }
;                 float Ag[4], Hg[4], Ao[4], Ho[4];
; #pragma unroll
;                 for (int g4 = 0; g4 < 4; ++g4) {
; #pragma unroll
;                     for (int j = 1; j < 4; ++j) { H[4 * g4 + j] = P[4 * g4 + j] * H[4 * g4 + j - 1] + H[4 * g4 + j]; P[4 * g4 + j] = P[4 * g4 + j] * P[4 * g4 + j - 1]; }
;                     Ag[g4] = P[4 * g4 + 3]; Hg[g4] = H[4 * g4 + 3]; Ao[g4] = get_x32(Ag[g4], hi); Ho[g4] = get_x32(Hg[g4], hi); }
;                 float C = carry[ct], PC = prodA[ct], Cm[4], Pm[4];
; #pragma unroll
;                 for (int g4 = 0; g4 < 4; ++g4) { const float A0 = hi ? Ao[g4] : Ag[g4], H0 = hi ? Ho[g4] : Hg[g4], A1 = hi ? Ag[g4] : Ao[g4], H1 = hi ? Hg[g4] : Ho[g4];
;                     const float C1 = A0 * C + H0, P1 = PC * A0; Cm[g4] = hi ? C1 : C; Pm[g4] = hi ? P1 : PC; C = A1 * C1 + H1; PC = P1 * A1; }
;                 carry[ct] = C; prodA[ct] = PC;
	v_exp_f32_e32 v23, v7
	v_pk_add_f32 v[36:37], v[36:37], 1.0 op_sel_hi:[1,0]
	v_pk_mul_f32 v[172:173], v[172:173], v[174:175]
	v_mul_f32_e32 v7, v36, v37
	v_rcp_f32_e32 v7, v7
	v_fma_f32 v3, -v23, v23, 1.0
	v_max_f32_e32 v3, 0, v3
	v_mov_b32_e32 v1, v169
	v_mul_f32_e32 v22, v37, v7
	v_mul_f32_e32 v22, v153, v22
	v_exp_f32_e32 v37, v22
	v_fmamk_f32 v22, v25, 0xbfb8aa3b, v203
	v_exp_f32_e32 v24, v22
	v_fmamk_f32 v22, v41, 0xbfb8aa3b, v204
	v_exp_f32_e32 v25, v22
	v_sqrt_f32_e32 v22, v3
	v_mul_f32_e32 v3, v36, v7
	v_mul_f32_e32 v40, v10, v3
	v_pk_add_f32 v[24:25], v[24:25], 1.0 op_sel_hi:[1,0]
	v_fmamk_f32 v3, v26, 0xbfb8aa3b, v203
	v_mul_f32_e32 v35, v24, v25
	v_rcp_f32_e32 v35, v35
	v_exp_f32_e32 v214, v3
	v_fmamk_f32 v3, v42, 0xbfb8aa3b, v204
	v_fma_f32 v7, -v37, v37, 1.0
	v_exp_f32_e32 v215, v3
	v_max_f32_e32 v7, 0, v7
	v_sqrt_f32_e32 v36, v7
	v_mul_f32_e32 v7, v25, v35
	v_mul_f32_e32 v7, v153, v7
	v_exp_f32_e32 v25, v7
	v_pk_add_f32 v[214:215], v[214:215], 1.0 op_sel_hi:[1,0]
	v_mul_f32_e32 v3, v24, v35
	v_mul_f32_e32 v7, v214, v215
	v_rcp_f32_e32 v7, v7
	v_fmamk_f32 v24, v27, 0xbfb8aa3b, v203
	v_exp_f32_e32 v26, v24
	v_fmamk_f32 v24, v43, 0xbfb8aa3b, v204
	v_fma_f32 v10, -v25, v25, 1.0
	v_exp_f32_e32 v27, v24
	v_max_f32_e32 v10, 0, v10
	v_sqrt_f32_e32 v217, v10
	v_mul_f32_e32 v10, v215, v7
	v_mul_f32_e32 v24, v214, v7
	v_mul_f32_e32 v7, v153, v10
	v_exp_f32_e32 v7, v7
	v_pk_add_f32 v[26:27], v[26:27], 1.0 op_sel_hi:[1,0]
	v_fma_f32 v16, -v17, v17, 1.0
	v_mul_f32_e32 v10, v26, v27
	v_rcp_f32_e32 v42, v10
	v_fma_f32 v10, -v7, v7, 1.0
	v_max_f32_e32 v10, 0, v10
	v_sqrt_f32_e32 v220, v10
	v_mul_f32_e32 v10, v27, v42
	v_mul_f32_e32 v10, v153, v10
	v_exp_f32_e32 v215, v10
	v_fmamk_f32 v10, v28, 0xbfb8aa3b, v203
	v_exp_f32_e32 v218, v10
	v_fmamk_f32 v10, v44, 0xbfb8aa3b, v204
	v_exp_f32_e32 v219, v10
	v_fma_f32 v10, -v215, v215, 1.0
	v_max_f32_e32 v10, 0, v10
	v_sqrt_f32_e32 v214, v10
	v_pk_add_f32 v[218:219], v[218:219], 1.0 op_sel_hi:[1,0]
	v_fmamk_f32 v27, v29, 0xbfb8aa3b, v203
	v_mul_f32_e32 v10, v218, v219
	v_rcp_f32_e32 v10, v10
	v_exp_f32_e32 v28, v27
	v_fmamk_f32 v27, v45, 0xbfb8aa3b, v204
	v_exp_f32_e32 v29, v27
	v_mul_f32_e32 v27, v219, v10
	v_mul_f32_e32 v27, v153, v27
	v_exp_f32_e32 v45, v27
	v_pk_add_f32 v[28:29], v[28:29], 1.0 op_sel_hi:[1,0]
	v_mul_f32_e32 v10, v218, v10
	v_mul_f32_e32 v27, v28, v29
	v_rcp_f32_e32 v27, v27
	v_mul_f32_e32 v14, v14, v10
	v_pk_mul_f32 v[0:1], v[0:1], v[172:173]
	v_max_f32_e32 v16, 0, v16
	v_mul_f32_e32 v10, v28, v27
	v_fma_f32 v35, -v45, v45, 1.0
	v_mul_f32_e32 v218, v15, v10
	v_mul_f32_e32 v10, v1, v47
	v_sqrt_f32_e32 v16, v16
	v_max_f32_e32 v35, 0, v35
	v_pk_fma_f32 v[172:173], v[0:1], v[46:47], v[10:11] op_sel_hi:[1,1,0]
	v_sqrt_f32_e32 v44, v35
	v_mov_b32_e32 v35, v172
	v_mul_f32_e32 v0, v172, v31
	v_pk_fma_f32 v[34:35], v[34:35], v[30:31], v[0:1] op_sel_hi:[1,1,0]
	v_fma_f32 v18, -v19, v19, 1.0
	v_mov_b32_e32 v177, v34
	v_max_f32_e32 v18, 0, v18
	v_pk_mul_f32 v[174:175], v[176:177], v[16:17]
	v_pk_mov_b32 v[4:5], v[4:5], v[4:5] op_sel:[1,0]
	v_sqrt_f32_e32 v18, v18
	v_fma_f32 v20, -v21, v21, 1.0
	v_add_f32_e32 v35, v174, v175
	v_mov_b32_e32 v179, v170
	v_mov_b32_e32 v181, v5
	v_max_f32_e32 v20, 0, v20
	v_mov_b32_e32 v0, v35
	v_mov_b32_e32 v10, v35
	v_pk_mul_f32 v[174:175], v[178:179], v[180:181]
	v_mov_b32_e32 v5, v193
	v_sqrt_f32_e32 v20, v20
	v_mul_f32_e32 v29, v29, v27
	v_permlane32_swap_b32_e32 v0, v10
	v_pk_mul_f32 v[4:5], v[4:5], v[174:175]
	v_mul_f32_e32 v29, v153, v29
	v_cndmask_b32_e64 v10, v0, v10, s[2:3]
	v_mul_f32_e32 v0, v5, v19
	v_exp_f32_e32 v29, v29
	v_pk_fma_f32 v[174:175], v[4:5], v[18:19], v[0:1] op_sel_hi:[1,1,0]
	v_pk_mov_b32 v[8:9], v[8:9], v[8:9] op_sel:[1,0]
	v_mov_b32_e32 v39, v174
	v_mul_f32_e32 v0, v174, v21
	v_pk_fma_f32 v[38:39], v[38:39], v[20:21], v[0:1] op_sel_hi:[1,1,0]
	v_fma_f32 v27, -v29, v29, 1.0
	v_mov_b32_e32 v209, v38
	v_pk_mul_f32 v[176:177], v[208:209], v[32:33]
	v_max_f32_e32 v27, 0, v27
	v_add_f32_e32 v4, v176, v177
	v_mov_b32_e32 v211, v207
	v_mov_b32_e32 v213, v9
	v_pk_mov_b32 v[12:13], v[12:13], v[12:13] op_sel:[1,0]
	v_sqrt_f32_e32 v28, v27
	v_mov_b32_e32 v0, v4
	v_mov_b32_e32 v15, v4
	v_pk_mul_f32 v[176:177], v[210:211], v[212:213]
	v_mov_b32_e32 v9, v216
	v_mov_b32_e32 v27, v24
	v_mov_b32_e32 v43, v13
	v_permlane32_swap_b32_e32 v0, v15
	v_pk_mul_f32 v[8:9], v[8:9], v[176:177]
	v_pk_mul_f32 v[26:27], v[26:27], v[42:43]
	v_mov_b32_e32 v13, v220
	v_cndmask_b32_e64 v16, v0, v15, s[2:3]
	v_mul_f32_e32 v0, v9, v23
	v_pk_mul_f32 v[12:13], v[12:13], v[26:27]
	v_pk_fma_f32 v[176:177], v[8:9], v[22:23], v[0:1] op_sel_hi:[1,1,0]
	v_mul_f32_e32 v0, v13, v215
	v_pk_fma_f32 v[26:27], v[12:13], v[214:215], v[0:1] op_sel_hi:[1,1,0]
	v_mov_b32_e32 v41, v176
	v_mov_b32_e32 v15, v26
	v_mul_f32_e32 v0, v26, v45
	v_pk_fma_f32 v[14:15], v[14:15], v[44:45], v[0:1] op_sel_hi:[1,1,0]
	v_mov_b32_e32 v214, v23
	v_pk_mul_f32 v[40:41], v[40:41], v[36:37]
	v_cndmask_b32_e64 v15, v10, v35, s[2:3]
	v_cndmask_b32_e64 v27, v35, v10, s[2:3]
	v_pk_mul_f32 v[22:23], v[214:215], v[6:7]
	v_mov_b32_e32 v10, v19
	v_mul_f32_e32 v46, v47, v165
	v_add_f32_e32 v8, v40, v41
	v_mov_b32_e32 v219, v14
	v_mul_f32_e32 v0, v14, v29
	v_mov_b32_e32 v36, v31
	v_mov_b32_e32 v47, v22
	v_mov_b32_e32 v44, v37
	v_pk_mul_f32 v[10:11], v[10:11], v[2:3]
	v_mov_b32_e32 v216, v21
	v_mul_f32_e32 v41, v25, v8
	v_pk_fma_f32 v[42:43], v[218:219], v[28:29], v[0:1] op_sel_hi:[1,1,0]
	v_pk_mul_f32 v[30:31], v[36:37], v[46:47]
	v_pk_mul_f32 v[36:37], v[44:45], v[22:23]
	v_mov_b32_e32 v24, v17
	v_pk_mul_f32 v[18:19], v[216:217], v[10:11]
	v_mov_b32_e32 v40, v33
	v_mov_b32_e32 v28, v25
	v_cndmask_b32_e64 v39, v16, v4, s[2:3]
; __device__ __forceinline__ float get_x32(float v, int hi) { const unsigned u = __builtin_bit_cast(unsigned, v); auto rr = __builtin_amdgcn_permlane32_swap(u, u, false, false); return __builtin_bit_cast(float, hi ? (unsigned)rr[0] : (unsigned)rr[1]); }
; __device__ __forceinline__ unsigned cvt_pk_bf16(float lo, float hi) { unsigned r; asm volatile("v_cvt_pk_bf16_f32 %0, %1, %2" : "=v"(r) : "v"(lo), "v"(hi)); return r; }
; __device__ __forceinline__ int crow(int r, int hi) { return (r & 3) + 8 * (r >> 2) + 4 * hi; }
; __device__ __forceinline__ int crow(int r, int hi) { return (r & 3) + 8 * (r >> 2) + 4 * hi; }
; __device__ __forceinline__ void lru_scan(LAS unsigned char* lds, const bf16* U, bf16* HR, bf16* PQ, float* AGG, const bf16* Wt, const float* conv_w, const float* conv_b,
;                                          const float* b_rg, const float* b_ig, const float* lam, int G, int c, int wbase) {
;     ...
;                 float Ag[4], Hg[4], Ao[4], Ho[4];
; #pragma unroll
;                 for (int g4 = 0; g4 < 4; ++g4) {
; #pragma unroll
;                     for (int j = 1; j < 4; ++j) { H[4 * g4 + j] = P[4 * g4 + j] * H[4 * g4 + j - 1] + H[4 * g4 + j]; P[4 * g4 + j] = P[4 * g4 + j] * P[4 * g4 + j - 1]; }
;                     Ag[g4] = P[4 * g4 + 3]; Hg[g4] = H[4 * g4 + 3]; Ao[g4] = get_x32(Ag[g4], hi); Ho[g4] = get_x32(Hg[g4], hi); }
;                 float C = carry[ct], PC = prodA[ct], Cm[4], Pm[4];
; #pragma unroll
;                 for (int g4 = 0; g4 < 4; ++g4) { const float A0 = hi ? Ao[g4] : Ag[g4], H0 = hi ? Ho[g4] : Hg[g4], A1 = hi ? Ag[g4] : Ao[g4], H1 = hi ? Hg[g4] : Ho[g4];
;                     const float C1 = A0 * C + H0, P1 = PC * A0; Cm[g4] = hi ? C1 : C; Pm[g4] = hi ? P1 : PC; C = A1 * C1 + H1; PC = P1 * A1; }
;                 carry[ct] = C; prodA[ct] = PC;
; #pragma unroll
;                 for (int r = 0; r < 16; r += 2) { const int o = crow(r, hi) * 64 + 32 * ct + r32;
;                     const unsigned wh = cvt_pk_bf16(H[r] + P[r] * Cm[r >> 2], H[r + 1] + P[r + 1] * Cm[r >> 2]), wp = cvt_pk_bf16(P[r] * Pm[r >> 2], P[r + 1] * Pm[r >> 2]);
;                     stH[o] = (bf16)(wh & 0xffffu); stH[o + 64] = (bf16)(wh >> 16); stP[o] = (bf16)(wp & 0xffffu); stP[o + 64] = (bf16)(wp >> 16); }
	v_cndmask_b32_e64 v169, v4, v16, s[2:3]
	v_pk_mul_f32 v[16:17], v[24:25], v[30:31]
	v_pk_mul_f32 v[20:21], v[40:41], v[18:19]
	v_pk_mul_f32 v[24:25], v[28:29], v[36:37]
	v_mov_b32_e32 v31, v16
	v_mov_b32_e32 v19, v24
	v_mov_b32_e32 v21, v24
	s_nop 1
	v_permlane32_swap_b32_e32 v19, v21
	v_cndmask_b32_e64 v19, v19, v21, s[2:3]
	v_mov_b32_e32 v21, v25
	v_mov_b32_e32 v28, v25
	v_mov_b32_e32 v43, v16
	v_pk_fma_f32 v[32:33], v[216:217], v[10:11], v[40:41]
	v_permlane32_swap_b32_e32 v21, v28
	v_permlane32_swap_b32_e32 v31, v43
	v_mov_b32_e32 v3, v20
	v_mov_b32_e32 v11, v20
	v_cndmask_b32_e64 v21, v21, v28, s[2:3]
	v_mov_b32_e32 v28, v33
	v_mov_b32_e32 v29, v33
	v_permlane32_swap_b32_e32 v3, v11
	v_cndmask_b32_e64 v31, v31, v43, s[2:3]
	v_permlane32_swap_b32_e32 v28, v29
	v_cndmask_b32_e64 v3, v3, v11, s[2:3]
	v_cndmask_b32_e64 v11, v28, v29, s[2:3]
	v_cndmask_b32_e64 v28, v31, v16, s[2:3]
	v_fmac_f32_e32 v15, v171, v28
	v_cndmask_b32_e64 v40, v16, v31, s[2:3]
	v_fmac_f32_e32 v27, v40, v15
	v_cndmask_b32_e64 v44, v3, v20, s[2:3]
	v_fmac_f32_e32 v39, v44, v27
	v_cndmask_b32_e64 v170, v20, v3, s[2:3]
	v_cndmask_b32_e64 v29, v19, v17, s[2:3]
	v_fmac_f32_e32 v169, v170, v39
	v_cndmask_b32_e64 v41, v11, v33, s[2:3]
	v_pk_mul_f32 v[180:181], v[168:169], v[28:29]
	v_mov_b32_e32 v0, v42
	v_mov_b32_e32 v12, v42
	v_cndmask_b32_e64 v3, v180, v168, s[2:3]
	v_pk_mul_f32 v[180:181], v[40:41], v[180:181]
	v_pk_fma_f32 v[28:29], v[168:169], v[28:29], v[40:41]
	v_permlane32_swap_b32_e32 v0, v12
	v_cndmask_b32_e64 v45, v24, v19, s[2:3]
	v_mov_b32_e32 v181, v29
	v_cndmask_b32_e64 v0, v0, v12, s[2:3]
	v_cndmask_b32_e64 v12, v15, v171, s[2:3]
	v_cndmask_b32_e64 v171, v33, v11, s[2:3]
	v_pk_mul_f32 v[208:209], v[44:45], v[180:181]
	v_mov_b32_e32 v40, v45
	v_cndmask_b32_e64 v17, v29, v169, s[2:3]
	v_pk_mul_f32 v[28:29], v[170:171], v[208:209]
	v_pk_fma_f32 v[44:45], v[44:45], v[180:181], v[170:171]
	v_cndmask_b32_e64 v179, v21, v25, s[2:3]
	v_cndmask_b32_e64 v178, v19, v24, s[2:3]
	v_mov_b32_e32 v29, v45
	v_cndmask_b32_e64 v41, v0, v42, s[2:3]
	v_pk_mul_f32 v[168:169], v[178:179], v[28:29]
	v_fmac_f32_e32 v1, v165, v12
	v_cndmask_b32_e64 v19, v168, v28, s[2:3]
	v_pk_fma_f32 v[28:29], v[178:179], v[28:29], v[40:41]
	v_cndmask_b32_e64 v11, v39, v27, s[2:3]
	v_cndmask_b32_e64 v15, v208, v180, s[2:3]
	v_fmac_f32_e32 v172, v46, v12
	v_cvt_pk_bf16_f32 v1, v1, v172
	v_mul_f32_e32 v27, v165, v3
	v_mul_f32_e32 v28, v46, v3
	v_fmac_f32_e32 v34, v30, v12
	v_fmac_f32_e32 v35, v16, v12
	v_mul_f32_e32 v12, v30, v3
	v_mul_f32_e32 v3, v16, v3
	v_cvt_pk_bf16_f32 v27, v27, v28
	ds_write_b16 v187, v1
	ds_write_b16_d16_hi v187, v1 offset:128
	ds_write_b16 v187, v27 offset:4096
	ds_write_b16_d16_hi v187, v27 offset:4224
	v_cvt_pk_bf16_f32 v1, v34, v35
	v_cvt_pk_bf16_f32 v3, v12, v3
	v_fmac_f32_e32 v5, v2, v11
	v_mul_f32_e32 v2, v2, v15
	ds_write_b16 v187, v1 offset:256
	ds_write_b16_d16_hi v187, v1 offset:384
	ds_write_b16 v187, v3 offset:4352
	ds_write_b16_d16_hi v187, v3 offset:4480
	v_fmac_f32_e32 v174, v10, v11
	v_cvt_pk_bf16_f32 v1, v5, v174
	v_mul_f32_e32 v3, v10, v15
	v_cvt_pk_bf16_f32 v2, v2, v3
	ds_write_b16 v187, v1 offset:1024
	ds_write_b16_d16_hi v187, v1 offset:1152
	ds_write_b16 v187, v2 offset:5120
	ds_write_b16_d16_hi v187, v2 offset:5248
	v_mul_f32_e32 v2, v18, v15
	v_fmac_f32_e32 v38, v18, v11
	v_fmac_f32_e32 v4, v20, v11
	v_cvt_pk_bf16_f32 v1, v38, v4
	v_mul_f32_e32 v3, v20, v15
	v_cvt_pk_bf16_f32 v2, v2, v3
	v_pk_mul_f32 v[208:209], v[40:41], v[168:169]
	ds_write_b16 v187, v1 offset:1280
	ds_write_b16_d16_hi v187, v1 offset:1408
	ds_write_b16 v187, v2 offset:5376
	ds_write_b16_d16_hi v187, v2 offset:5504
	v_mul_f32_e32 v2, v6, v19
	v_cndmask_b32_e64 v181, v25, v21, s[2:3]
	v_mov_b32_e32 v180, v179
	v_mov_b32_e32 v209, v29
	v_fmac_f32_e32 v9, v6, v17
	v_fmac_f32_e32 v176, v22, v17
	v_cvt_pk_bf16_f32 v1, v9, v176
	v_mul_f32_e32 v3, v22, v19
	v_cvt_pk_bf16_f32 v2, v2, v3
	v_pk_mul_f32 v[178:179], v[180:181], v[208:209]
	ds_write_b16 v187, v1 offset:2048
	ds_write_b16_d16_hi v187, v1 offset:2176
	ds_write_b16 v187, v2 offset:6144
	ds_write_b16_d16_hi v187, v2 offset:6272
	v_mul_f32_e32 v2, v36, v19
	v_cndmask_b32_e64 v177, v42, v0, s[2:3]
	v_cndmask_b32_e64 v0, v29, v45, s[2:3]
	v_cndmask_b32_e64 v21, v178, v208, s[2:3]
	v_fmac_f32_e32 v8, v36, v17
	v_fmac_f32_e32 v33, v24, v17
	v_cvt_pk_bf16_f32 v1, v8, v33
	v_mul_f32_e32 v3, v24, v19
	v_cvt_pk_bf16_f32 v2, v2, v3
	ds_write_b16 v187, v1 offset:2304
	ds_write_b16_d16_hi v187, v1 offset:2432
	ds_write_b16 v187, v2 offset:6400
	ds_write_b16_d16_hi v187, v2 offset:6528
	v_fmac_f32_e32 v13, v7, v0
	v_fmac_f32_e32 v26, v23, v0
	v_cvt_pk_bf16_f32 v1, v13, v26
	v_mul_f32_e32 v2, v7, v21
	v_mul_f32_e32 v3, v23, v21
	v_cvt_pk_bf16_f32 v2, v2, v3
	ds_write_b16 v187, v1 offset:3072
	ds_write_b16_d16_hi v187, v1 offset:3200
	ds_write_b16 v187, v2 offset:7168
	ds_write_b16_d16_hi v187, v2 offset:7296
	v_fmac_f32_e32 v14, v37, v0
	v_fmac_f32_e32 v42, v25, v0
	v_cvt_pk_bf16_f32 v0, v14, v42
	v_mul_f32_e32 v1, v37, v21
	v_mul_f32_e32 v2, v25, v21
	v_cvt_pk_bf16_f32 v1, v1, v2
	ds_write_b16 v187, v0 offset:3328
	ds_write_b16_d16_hi v187, v0 offset:3456
	ds_write_b16 v187, v1 offset:7424
	ds_write_b16_d16_hi v187, v1 offset:7552
	v_mov_b32 v0, 0
	v_mov_b32_e32 v176, v181
	v_add_u32_e32 v165, v199, v0
	ds_read_b128 v[0:3], v165
	ds_read_b128 v[168:171], v165 offset:32
	s_waitcnt lgkmcnt(1)
	v_mfma_f32_32x32x16_bf16 v[16:31], v[124:127], v[0:3], 0
	ds_read_b128 v[0:3], v165 offset:9216
	ds_read_b128 v[172:175], v165 offset:9248
	s_waitcnt lgkmcnt(1)
; #define LAS __attribute__((address_space(3)))
; __device__ __forceinline__ void lru_scan(LAS unsigned char* lds, const bf16* U, bf16* HR, bf16* PQ, float* AGG, const bf16* Wt, const float* conv_w, const float* conv_b,
;                                          const float* b_rg, const float* b_ig, const float* lam, int G, int c, int wbase) {
;     ...
;             for (int ct = 0; ct < 2; ++ct) {
;                 f32x16 R = {}, I = {}, X = {};
;                 int zoff; asm volatile("v_mov_b32 %0, 0" : "=v"(zoff)); const LAS unsigned char* Wp = lds + WL_OFF + zoff;
;                 bf16x8 wr[4], wi[4];
; #pragma unroll
;                 for (int ks = 0; ks < 4; ++ks) { const int o = (32 * ct + r32) * WL_ROW + (16 * ks + 8 * hi) * 2; wr[ks] = *(const LAS bf16x8*)(Wp + o); wi[ks] = *(const LAS bf16x8*)(Wp + 64 * WL_ROW + o); }
; #pragma unroll
;                 for (int ks = 0; ks < 4; ++ks) { bf16x8 idf;
; #pragma unroll
;                     for (int j = 0; j < 8; ++j) idf[j] = (16 * ks + 8 * hi + j == 32 * ct + r32) ? (short)0x3F80 : (short)0;
;                     R = __builtin_amdgcn_mfma_f32_32x32x16_bf16(af[ks], wr[ks], R, 0, 0, 0); I = __builtin_amdgcn_mfma_f32_32x32x16_bf16(af[ks], wi[ks], I, 0, 0, 0);
;                     X = __builtin_amdgcn_mfma_f32_32x32x16_bf16(af[ks], idf, X, 0, 0, 0); }
;                 float P[16], H[16];
; #pragma unroll
;                 for (int r = 0; r < 16; ++r) { const float er = __builtin_amdgcn_exp2f(R[r] * -LOG2E + brg[ct]), ei = __builtin_amdgcn_exp2f(I[r] * -LOG2E + big[ct]);
;                     const float e1 = 1.f + er, e2 = 1.f + ei, qq = __builtin_amdgcn_rcpf(e1 * e2), rr = qq * e2, ii = qq * e1;
;                     const float a = __builtin_amdgcn_exp2f(rr * sp8[ct]);
;                     P[r] = a; H[r] = __builtin_amdgcn_sqrtf(fmaxf(1.f - a * a, 0.f)) * (ii * X[r]); }
	v_mfma_f32_32x32x16_bf16 v[32:47], v[124:127], v[0:3], 0
	v_mfma_f32_32x32x16_bf16 v[0:15], v[124:127], v[140:143], 0
	v_mfma_f32_32x32x16_bf16 v[16:31], v[128:131], v[168:171], v[16:31]
	v_mul_f32_e64 v168, v176, v178
	v_mul_f32_e64 v169, v177, v179
	v_fma_f32 v170, v180, v208, v176
	v_fma_f32 v171, v181, v209, v177
	s_waitcnt lgkmcnt(0)
	v_mfma_f32_32x32x16_bf16 v[32:47], v[128:131], v[172:175], v[32:47]
	v_mfma_f32_32x32x16_bf16 v[0:15], v[128:131], v[140:143], v[0:15]
	ds_read_b128 v[124:127], v165 offset:64
	ds_read_b128 v[128:131], v165 offset:96
	s_waitcnt lgkmcnt(1)
	v_mfma_f32_32x32x16_bf16 v[16:31], v[132:135], v[124:127], v[16:31]
	ds_read_b128 v[124:127], v165 offset:9280
	ds_read_b128 v[140:143], v165 offset:9312
	s_waitcnt lgkmcnt(1)
	v_mfma_f32_32x32x16_bf16 v[32:47], v[132:135], v[124:127], v[32:47]
	v_mfma_f32_32x32x16_bf16 v[16:31], v[136:139], v[128:131], v[16:31]
	s_waitcnt lgkmcnt(0)
	v_mfma_f32_32x32x16_bf16 v[32:47], v[136:139], v[140:143], v[32:47]
	s_nop 9
	v_fmamk_f32 v16, v16, 0xbfb8aa3b, v192
	v_exp_f32_e32 v124, v16
	v_fmamk_f32 v20, v20, 0xbfb8aa3b, v192
	v_fmamk_f32 v23, v23, 0xbfb8aa3b, v192
	v_fmamk_f32 v24, v24, 0xbfb8aa3b, v192
	v_fmamk_f32 v16, v32, 0xbfb8aa3b, v202
	v_exp_f32_e32 v125, v16
	v_mfma_f32_32x32x16_bf16 v[0:15], v[132:135], v[48:51], v[0:15]
	v_add_f32_e64 v124, v124, 1.0
	v_add_f32_e64 v125, v125, 1.0
	v_mul_f32_e32 v16, v124, v125
	v_rcp_f32_e32 v16, v16
	s_nop 0
	v_mul_f32_e32 v32, v125, v16
	v_mul_f32_e32 v127, v124, v16
	v_mul_f32_e32 v16, v206, v32
	v_exp_f32_e32 v134, v16
	v_fmamk_f32 v16, v17, 0xbfb8aa3b, v192
	v_fmamk_f32 v17, v33, 0xbfb8aa3b, v202
	v_exp_f32_e32 v16, v16
	v_exp_f32_e32 v17, v17
	v_fma_f32 v32, -v134, v134, 1.0
	v_max_f32_e32 v32, 0, v32
	v_sqrt_f32_e32 v133, v32
	v_pk_add_f32 v[124:125], v[16:17], 1.0 op_sel_hi:[1,0]
	v_fmamk_f32 v17, v34, 0xbfb8aa3b, v202
	v_mul_f32_e32 v16, v124, v125
	v_rcp_f32_e32 v126, v16
	v_fmamk_f32 v16, v18, 0xbfb8aa3b, v192
	v_exp_f32_e32 v16, v16
	v_exp_f32_e32 v17, v17
	v_mul_f32_e32 v18, v125, v126
	v_mul_f32_e32 v18, v206, v18
	v_exp_f32_e32 v129, v18
	v_pk_add_f32 v[16:17], v[16:17], 1.0 op_sel_hi:[1,0]
	v_mfma_f32_32x32x16_bf16 v[0:15], v[136:139], v[56:59], v[0:15]
	v_mul_f32_e32 v18, v16, v17
	v_rcp_f32_e32 v32, v18
	v_fma_f32 v18, -v129, v129, 1.0
	v_max_f32_e32 v18, 0, v18
	v_sqrt_f32_e32 v128, v18
	v_fmamk_f32 v18, v19, 0xbfb8aa3b, v192
	v_fmamk_f32 v19, v35, 0xbfb8aa3b, v202
	v_mul_f32_e32 v17, v17, v32
	v_exp_f32_e32 v18, v18
	v_exp_f32_e32 v19, v19
	v_mul_f32_e32 v34, v16, v32
	v_exp_f32_e32 v32, v20
	v_fmamk_f32 v20, v36, 0xbfb8aa3b, v202
	v_exp_f32_e32 v33, v20
	v_mul_f32_e32 v16, v206, v17
	v_pk_add_f32 v[18:19], v[18:19], 1.0 op_sel_hi:[1,0]
	v_exp_f32_e32 v17, v16
	v_mul_f32_e32 v16, v18, v19
	v_pk_add_f32 v[32:33], v[32:33], 1.0 op_sel_hi:[1,0]
	v_rcp_f32_e32 v35, v16
	v_mul_f32_e32 v20, v32, v33
	v_rcp_f32_e32 v20, v20
	v_mul_f32_e32 v34, v2, v34
	v_mul_f32_e32 v2, v18, v35
	v_mul_f32_e32 v36, v3, v2
	v_mul_f32_e32 v2, v33, v20
	v_mul_f32_e32 v2, v206, v2
	v_fmamk_f32 v3, v21, 0xbfb8aa3b, v192
	v_mul_f32_e32 v135, v32, v20
	v_exp_f32_e32 v2, v2
	v_exp_f32_e32 v20, v3
	v_fmamk_f32 v3, v37, 0xbfb8aa3b, v202
	v_exp_f32_e32 v21, v3
	v_fma_f32 v3, -v2, v2, 1.0
	v_max_f32_e32 v3, 0, v3
	v_sqrt_f32_e32 v137, v3
	v_pk_add_f32 v[130:131], v[20:21], 1.0 op_sel_hi:[1,0]
	v_mul_f32_e32 v19, v19, v35
	v_mul_f32_e32 v3, v130, v131
	v_rcp_f32_e32 v132, v3
	v_fmamk_f32 v3, v22, 0xbfb8aa3b, v192
	v_exp_f32_e32 v32, v3
	v_fmamk_f32 v3, v38, 0xbfb8aa3b, v202
	v_exp_f32_e32 v33, v3
	v_mul_f32_e32 v3, v131, v132
	v_mul_f32_e32 v3, v206, v3
	v_exp_f32_e32 v21, v3
	v_pk_add_f32 v[32:33], v[32:33], 1.0 op_sel_hi:[1,0]
	v_exp_f32_e32 v38, v23
	v_mul_f32_e32 v3, v32, v33
	v_rcp_f32_e32 v3, v3
	v_fmamk_f32 v23, v39, 0xbfb8aa3b, v202
	v_exp_f32_e32 v39, v23
	v_mul_f32_e32 v19, v206, v19
	v_mul_f32_e32 v22, v33, v3
	v_mul_f32_e32 v3, v32, v3
	v_mul_f32_e32 v22, v206, v22
	v_pk_add_f32 v[32:33], v[38:39], 1.0 op_sel_hi:[1,0]
	v_exp_f32_e32 v23, v22
	v_mul_f32_e32 v22, v32, v33
	v_exp_f32_e32 v38, v24
	v_fmamk_f32 v24, v40, 0xbfb8aa3b, v202
	v_rcp_f32_e32 v35, v22
	v_exp_f32_e32 v39, v24
	v_mul_f32_e32 v40, v6, v3
	v_exp_f32_e32 v19, v19
	v_mul_f32_e32 v33, v33, v35
	v_pk_add_f32 v[38:39], v[38:39], 1.0 op_sel_hi:[1,0]
	v_mul_f32_e32 v33, v206, v33
	v_mul_f32_e32 v24, v38, v39
	v_exp_f32_e32 v33, v33
	v_mul_f32_e32 v3, v32, v35
	v_rcp_f32_e32 v35, v24
	v_mul_f32_e32 v136, v7, v3
	v_fma_f32 v6, -v33, v33, 1.0
	v_max_f32_e32 v6, 0, v6
	v_mul_f32_e32 v3, v39, v35
	v_mul_f32_e32 v3, v206, v3
	v_sqrt_f32_e32 v32, v6
	v_exp_f32_e32 v6, v3
	v_fmamk_f32 v3, v25, 0xbfb8aa3b, v192
	v_exp_f32_e32 v24, v3
	v_fmamk_f32 v3, v41, 0xbfb8aa3b, v202
	v_exp_f32_e32 v25, v3
	v_mul_f32_e32 v141, v38, v35
	v_fma_f32 v3, -v6, v6, 1.0
	v_max_f32_e32 v3, 0, v3
	v_pk_add_f32 v[138:139], v[24:25], 1.0 op_sel_hi:[1,0]
	v_sqrt_f32_e32 v165, v3
	v_mul_f32_e32 v7, v138, v139
	v_rcp_f32_e32 v140, v7
	v_fmamk_f32 v7, v26, 0xbfb8aa3b, v192
	v_exp_f32_e32 v38, v7
	v_fmamk_f32 v7, v42, 0xbfb8aa3b, v202
	v_exp_f32_e32 v39, v7
	v_mul_f32_e32 v7, v139, v140
	v_mul_f32_e32 v7, v206, v7
	v_exp_f32_e32 v25, v7
	v_pk_add_f32 v[38:39], v[38:39], 1.0 op_sel_hi:[1,0]
	v_pk_mov_b32 v[0:1], v[0:1], v[0:1] op_sel:[1,0]
	v_mul_f32_e32 v7, v38, v39
	v_rcp_f32_e32 v7, v7
	v_fma_f32 v3, -v25, v25, 1.0
	v_max_f32_e32 v3, 0, v3
	v_fma_f32 v16, -v17, v17, 1.0
	v_mul_f32_e32 v24, v39, v7
	v_mul_f32_e32 v24, v206, v24
	v_exp_f32_e32 v39, v24
	v_fmamk_f32 v24, v27, 0xbfb8aa3b, v192
	v_exp_f32_e32 v26, v24
	v_fmamk_f32 v24, v43, 0xbfb8aa3b, v202
	v_exp_f32_e32 v27, v24
	v_sqrt_f32_e32 v24, v3
; __device__ __forceinline__ float get_x32(float v, int hi) { const unsigned u = __builtin_bit_cast(unsigned, v); auto rr = __builtin_amdgcn_permlane32_swap(u, u, false, false); return __builtin_bit_cast(float, hi ? (unsigned)rr[0] : (unsigned)rr[1]); }
; __device__ __forceinline__ void lru_scan(LAS unsigned char* lds, const bf16* U, bf16* HR, bf16* PQ, float* AGG, const bf16* Wt, const float* conv_w, const float* conv_b,
;                                          const float* b_rg, const float* b_ig, const float* lam, int G, int c, int wbase) {
;     ...
;                 for (int r = 0; r < 16; ++r) { const float er = __builtin_amdgcn_exp2f(R[r] * -LOG2E + brg[ct]), ei = __builtin_amdgcn_exp2f(I[r] * -LOG2E + big[ct]);
;                     const float e1 = 1.f + er, e2 = 1.f + ei, qq = __builtin_amdgcn_rcpf(e1 * e2), rr = qq * e2, ii = qq * e1;
;                     const float a = __builtin_amdgcn_exp2f(rr * sp8[ct]);
;                     P[r] = a; H[r] = __builtin_amdgcn_sqrtf(fmaxf(1.f - a * a, 0.f)) * (ii * X[r]); }
;                 float Ag[4], Hg[4], Ao[4], Ho[4];
; #pragma unroll
;                 for (int g4 = 0; g4 < 4; ++g4) {
; #pragma unroll
;                     for (int j = 1; j < 4; ++j) { H[4 * g4 + j] = P[4 * g4 + j] * H[4 * g4 + j - 1] + H[4 * g4 + j]; P[4 * g4 + j] = P[4 * g4 + j] * P[4 * g4 + j - 1]; }
;                     Ag[g4] = P[4 * g4 + 3]; Hg[g4] = H[4 * g4 + 3]; Ao[g4] = get_x32(Ag[g4], hi); Ho[g4] = get_x32(Hg[g4], hi); }
;                 float C = carry[ct], PC = prodA[ct], Cm[4], Pm[4];
; #pragma unroll
;                 for (int g4 = 0; g4 < 4; ++g4) { const float A0 = hi ? Ao[g4] : Ag[g4], H0 = hi ? Ho[g4] : Hg[g4], A1 = hi ? Ag[g4] : Ao[g4], H1 = hi ? Hg[g4] : Ho[g4];
;                     const float C1 = A0 * C + H0, P1 = PC * A0; Cm[g4] = hi ? C1 : C; Pm[g4] = hi ? P1 : PC; C = A1 * C1 + H1; PC = P1 * A1; }
;                 carry[ct] = C; prodA[ct] = PC;
	v_mul_f32_e32 v3, v38, v7
	v_mul_f32_e32 v42, v10, v3
	v_pk_add_f32 v[26:27], v[26:27], 1.0 op_sel_hi:[1,0]
	v_fmamk_f32 v3, v28, 0xbfb8aa3b, v192
	v_mul_f32_e32 v35, v26, v27
	v_rcp_f32_e32 v35, v35
	v_exp_f32_e32 v142, v3
	v_fmamk_f32 v3, v44, 0xbfb8aa3b, v202
	v_fma_f32 v7, -v39, v39, 1.0
	v_exp_f32_e32 v143, v3
	v_max_f32_e32 v7, 0, v7
	v_sqrt_f32_e32 v38, v7
	v_mul_f32_e32 v7, v27, v35
	v_mul_f32_e32 v7, v206, v7
	v_exp_f32_e32 v27, v7
	v_pk_add_f32 v[142:143], v[142:143], 1.0 op_sel_hi:[1,0]
	v_mul_f32_e32 v3, v26, v35
	v_mul_f32_e32 v7, v142, v143
	v_rcp_f32_e32 v7, v7
	v_fmamk_f32 v26, v29, 0xbfb8aa3b, v192
	v_exp_f32_e32 v28, v26
	v_fmamk_f32 v26, v45, 0xbfb8aa3b, v202
	v_fma_f32 v10, -v27, v27, 1.0
	v_exp_f32_e32 v29, v26
	v_max_f32_e32 v10, 0, v10
	v_sqrt_f32_e32 v173, v10
	v_mul_f32_e32 v10, v143, v7
	v_mul_f32_e32 v26, v142, v7
	v_mul_f32_e32 v7, v206, v10
	v_exp_f32_e32 v7, v7
	v_pk_add_f32 v[28:29], v[28:29], 1.0 op_sel_hi:[1,0]
	v_mov_b32_e32 v125, v127
	v_mul_f32_e32 v10, v28, v29
	v_rcp_f32_e32 v44, v10
	v_fma_f32 v10, -v7, v7, 1.0
	v_max_f32_e32 v10, 0, v10
	v_sqrt_f32_e32 v166, v10
	v_mul_f32_e32 v10, v29, v44
	v_mul_f32_e32 v10, v206, v10
	v_exp_f32_e32 v143, v10
	v_fmamk_f32 v10, v30, 0xbfb8aa3b, v192
	v_exp_f32_e32 v174, v10
	v_fmamk_f32 v10, v46, 0xbfb8aa3b, v202
	v_exp_f32_e32 v175, v10
	v_fma_f32 v10, -v143, v143, 1.0
	v_max_f32_e32 v10, 0, v10
	v_sqrt_f32_e32 v142, v10
	v_pk_add_f32 v[174:175], v[174:175], 1.0 op_sel_hi:[1,0]
	v_fmamk_f32 v29, v31, 0xbfb8aa3b, v192
	v_mul_f32_e32 v10, v174, v175
	v_rcp_f32_e32 v10, v10
	v_exp_f32_e32 v30, v29
	v_fmamk_f32 v29, v47, 0xbfb8aa3b, v202
	v_exp_f32_e32 v31, v29
	v_mul_f32_e32 v29, v175, v10
	v_mul_f32_e32 v29, v206, v29
	v_exp_f32_e32 v47, v29
	v_pk_add_f32 v[30:31], v[30:31], 1.0 op_sel_hi:[1,0]
	v_mov_b32_e32 v127, v1
	v_mul_f32_e32 v29, v30, v31
	v_rcp_f32_e32 v29, v29
	v_max_f32_e32 v16, 0, v16
	v_mul_f32_e32 v10, v174, v10
	v_pk_mul_f32 v[124:125], v[124:125], v[126:127]
	v_mov_b32_e32 v1, v133
	v_sqrt_f32_e32 v16, v16
	v_fma_f32 v18, -v19, v19, 1.0
	v_mul_f32_e32 v14, v14, v10
	v_mul_f32_e32 v10, v30, v29
	v_pk_mul_f32 v[0:1], v[0:1], v[124:125]
	v_max_f32_e32 v18, 0, v18
	v_fma_f32 v35, -v47, v47, 1.0
	v_mul_f32_e32 v174, v15, v10
	v_mul_f32_e32 v10, v1, v129
	v_sqrt_f32_e32 v18, v18
	v_max_f32_e32 v35, 0, v35
	v_pk_fma_f32 v[124:125], v[0:1], v[128:129], v[10:11] op_sel_hi:[1,1,0]
	v_sqrt_f32_e32 v46, v35
	v_mov_b32_e32 v35, v124
	v_mul_f32_e32 v0, v124, v17
	v_pk_fma_f32 v[34:35], v[34:35], v[16:17], v[0:1] op_sel_hi:[1,1,0]
	v_fma_f32 v20, -v21, v21, 1.0
	v_mov_b32_e32 v37, v34
	v_max_f32_e32 v20, 0, v20
	v_pk_mul_f32 v[36:37], v[36:37], v[18:19]
	v_pk_mov_b32 v[4:5], v[4:5], v[4:5] op_sel:[1,0]
	v_sqrt_f32_e32 v20, v20
	v_fma_f32 v22, -v23, v23, 1.0
	v_add_f32_e32 v35, v36, v37
	v_mov_b32_e32 v131, v135
	v_mov_b32_e32 v133, v5
	v_max_f32_e32 v22, 0, v22
	v_mov_b32_e32 v0, v35
	v_mov_b32_e32 v10, v35
	v_pk_mul_f32 v[36:37], v[130:131], v[132:133]
	v_mov_b32_e32 v5, v137
	v_sqrt_f32_e32 v22, v22
	v_mul_f32_e32 v31, v31, v29
	v_permlane32_swap_b32_e32 v0, v10
	v_pk_mul_f32 v[4:5], v[4:5], v[36:37]
	v_mul_f32_e32 v31, v206, v31
	v_cndmask_b32_e64 v10, v0, v10, s[2:3]
	v_mul_f32_e32 v0, v5, v21
	v_exp_f32_e32 v31, v31
	v_pk_fma_f32 v[36:37], v[4:5], v[20:21], v[0:1] op_sel_hi:[1,1,0]
	v_mul_f32_e32 v126, v129, v134
	v_mov_b32_e32 v41, v36
	v_mul_f32_e32 v0, v36, v23
	v_pk_fma_f32 v[40:41], v[40:41], v[22:23], v[0:1] op_sel_hi:[1,1,0]
	v_fma_f32 v29, -v31, v31, 1.0
	v_mov_b32_e32 v137, v40
	v_pk_mul_f32 v[128:129], v[136:137], v[32:33]
	v_pk_mov_b32 v[8:9], v[8:9], v[8:9] op_sel:[1,0]
	v_max_f32_e32 v29, 0, v29
	v_add_f32_e32 v4, v128, v129
	v_mov_b32_e32 v139, v141
	v_mov_b32_e32 v141, v9
	v_pk_mov_b32 v[12:13], v[12:13], v[12:13] op_sel:[1,0]
	v_sqrt_f32_e32 v30, v29
	v_mov_b32_e32 v0, v4
	v_mov_b32_e32 v15, v4
	v_pk_mul_f32 v[128:129], v[138:139], v[140:141]
	v_mov_b32_e32 v9, v165
	v_mov_b32_e32 v29, v26
	v_mov_b32_e32 v45, v13
	v_permlane32_swap_b32_e32 v0, v15
	v_pk_mul_f32 v[8:9], v[8:9], v[128:129]
	v_pk_mul_f32 v[28:29], v[28:29], v[44:45]
	v_mov_b32_e32 v13, v166
	v_cndmask_b32_e64 v16, v0, v15, s[2:3]
	v_mul_f32_e32 v0, v9, v25
	v_pk_mul_f32 v[12:13], v[12:13], v[28:29]
	v_pk_fma_f32 v[128:129], v[8:9], v[24:25], v[0:1] op_sel_hi:[1,1,0]
	v_mul_f32_e32 v0, v13, v143
	v_pk_fma_f32 v[28:29], v[12:13], v[142:143], v[0:1] op_sel_hi:[1,1,0]
	v_mov_b32_e32 v43, v128
	v_mov_b32_e32 v15, v28
	v_mul_f32_e32 v0, v28, v47
	v_pk_fma_f32 v[14:15], v[14:15], v[46:47], v[0:1] op_sel_hi:[1,1,0]
	v_mov_b32_e32 v142, v25
	v_pk_mul_f32 v[42:43], v[42:43], v[38:39]
	v_cndmask_b32_e64 v15, v10, v35, s[2:3]
	v_cndmask_b32_e64 v29, v35, v10, s[2:3]
	v_pk_mul_f32 v[24:25], v[142:143], v[6:7]
	v_mov_b32_e32 v10, v21
	v_add_f32_e32 v8, v42, v43
	v_mov_b32_e32 v175, v14
	v_mul_f32_e32 v0, v14, v31
	v_mov_b32_e32 v38, v17
	v_mov_b32_e32 v127, v24
	v_mov_b32_e32 v46, v39
	v_pk_mul_f32 v[10:11], v[10:11], v[2:3]
	v_mov_b32_e32 v172, v23
	v_mul_f32_e32 v43, v27, v8
	v_pk_fma_f32 v[44:45], v[174:175], v[30:31], v[0:1] op_sel_hi:[1,1,0]
	v_cndmask_b32_e64 v37, v16, v4, s[2:3]
	v_cndmask_b32_e64 v165, v4, v16, s[2:3]
	v_pk_mul_f32 v[16:17], v[38:39], v[126:127]
	v_pk_mul_f32 v[38:39], v[46:47], v[24:25]
	v_mov_b32_e32 v26, v19
	v_pk_mul_f32 v[20:21], v[172:173], v[10:11]
	v_mov_b32_e32 v42, v33
	v_mov_b32_e32 v30, v27
	v_pk_mul_f32 v[18:19], v[26:27], v[16:17]
	v_pk_mul_f32 v[22:23], v[42:43], v[20:21]
	v_pk_mul_f32 v[26:27], v[30:31], v[38:39]
	v_mov_b32_e32 v17, v18
	v_mov_b32_e32 v21, v26
	v_mov_b32_e32 v23, v26
	s_nop 1
	v_permlane32_swap_b32_e32 v21, v23
	v_cndmask_b32_e64 v21, v21, v23, s[2:3]
; #define LAS __attribute__((address_space(3)))
; __device__ __forceinline__ float get_x32(float v, int hi) { const unsigned u = __builtin_bit_cast(unsigned, v); auto rr = __builtin_amdgcn_permlane32_swap(u, u, false, false); return __builtin_bit_cast(float, hi ? (unsigned)rr[0] : (unsigned)rr[1]); }
; __device__ __forceinline__ int crow(int r, int hi) { return (r & 3) + 8 * (r >> 2) + 4 * hi; }
; __device__ __forceinline__ void lru_scan(LAS unsigned char* lds, const bf16* U, bf16* HR, bf16* PQ, float* AGG, const bf16* Wt, const float* conv_w, const float* conv_b,
;                                          const float* b_rg, const float* b_ig, const float* lam, int G, int c, int wbase) {
;     ...
;                     for (int j = 1; j < 4; ++j) { H[4 * g4 + j] = P[4 * g4 + j] * H[4 * g4 + j - 1] + H[4 * g4 + j]; P[4 * g4 + j] = P[4 * g4 + j] * P[4 * g4 + j - 1]; }
;                     Ag[g4] = P[4 * g4 + 3]; Hg[g4] = H[4 * g4 + 3]; Ao[g4] = get_x32(Ag[g4], hi); Ho[g4] = get_x32(Hg[g4], hi); }
;                 float C = carry[ct], PC = prodA[ct], Cm[4], Pm[4];
; #pragma unroll
;                 for (int g4 = 0; g4 < 4; ++g4) { const float A0 = hi ? Ao[g4] : Ag[g4], H0 = hi ? Ho[g4] : Hg[g4], A1 = hi ? Ag[g4] : Ao[g4], H1 = hi ? Hg[g4] : Ho[g4];
;                     const float C1 = A0 * C + H0, P1 = PC * A0; Cm[g4] = hi ? C1 : C; Pm[g4] = hi ? P1 : PC; C = A1 * C1 + H1; PC = P1 * A1; }
;                 carry[ct] = C; prodA[ct] = PC;
; #pragma unroll
;                 for (int r = 0; r < 16; r += 2) { const int o = crow(r, hi) * 64 + 32 * ct + r32;
;                     const unsigned wh = cvt_pk_bf16(H[r] + P[r] * Cm[r >> 2], H[r + 1] + P[r + 1] * Cm[r >> 2]), wp = cvt_pk_bf16(P[r] * Pm[r >> 2], P[r + 1] * Pm[r >> 2]);
;                     stH[o] = (bf16)(wh & 0xffffu); stH[o + 64] = (bf16)(wh >> 16); stP[o] = (bf16)(wp & 0xffffu); stP[o + 64] = (bf16)(wp >> 16); }
;             }
;             asm volatile("s_waitcnt lgkmcnt(0)" ::: "memory");
; #pragma unroll
;             for (int i = 0; i < 4; ++i) { const int row = (lane >> 3) + 8 * i, chn = lane & 7; const size_t go = ((size_t)b * SEQ + t0 + row) * DM + ch0 + 8 * chn;
;                 *(u32x4*)(HR + go) = *(const LAS u32x4*)(stH + row * 64 + 8 * chn); *(u32x4*)(PQ + go) = *(const LAS u32x4*)(stP + row * 64 + 8 * chn); }
;             asm volatile("s_waitcnt lgkmcnt(0)" ::: "memory");
	v_mov_b32_e32 v23, v27
	v_mov_b32_e32 v30, v27
	v_mov_b32_e32 v41, v18
	v_pk_fma_f32 v[32:33], v[172:173], v[10:11], v[42:43]
	v_permlane32_swap_b32_e32 v23, v30
	v_permlane32_swap_b32_e32 v17, v41
	v_mov_b32_e32 v3, v22
	v_mov_b32_e32 v11, v22
	v_cndmask_b32_e64 v23, v23, v30, s[2:3]
	v_mov_b32_e32 v30, v33
	v_mov_b32_e32 v31, v33
	v_permlane32_swap_b32_e32 v3, v11
	v_cndmask_b32_e64 v17, v17, v41, s[2:3]
	v_permlane32_swap_b32_e32 v30, v31
	v_cndmask_b32_e64 v3, v3, v11, s[2:3]
	v_cndmask_b32_e64 v11, v30, v31, s[2:3]
	v_cndmask_b32_e64 v30, v17, v18, s[2:3]
	v_fmac_f32_e32 v15, v167, v30
	v_cndmask_b32_e64 v42, v18, v17, s[2:3]
	v_fmac_f32_e32 v29, v42, v15
	v_cndmask_b32_e64 v46, v3, v22, s[2:3]
	v_fmac_f32_e32 v37, v46, v29
	v_cndmask_b32_e64 v130, v22, v3, s[2:3]
	v_cndmask_b32_e64 v31, v21, v19, s[2:3]
	v_fmac_f32_e32 v165, v130, v37
	v_mov_b32_e32 v0, v44
	v_mov_b32_e32 v12, v44
	v_cndmask_b32_e64 v43, v11, v33, s[2:3]
	v_pk_mul_f32 v[136:137], v[164:165], v[30:31]
	v_permlane32_swap_b32_e32 v0, v12
	v_cndmask_b32_e64 v3, v136, v164, s[2:3]
	v_pk_mul_f32 v[136:137], v[42:43], v[136:137]
	v_pk_fma_f32 v[30:31], v[164:165], v[30:31], v[42:43]
	v_cndmask_b32_e64 v0, v0, v12, s[2:3]
	v_cndmask_b32_e64 v12, v15, v167, s[2:3]
	v_cndmask_b32_e64 v47, v26, v21, s[2:3]
	v_mov_b32_e32 v137, v31
	v_cndmask_b32_e64 v131, v33, v11, s[2:3]
	v_pk_mul_f32 v[138:139], v[46:47], v[136:137]
	v_fmac_f32_e32 v1, v134, v12
	v_cndmask_b32_e64 v133, v23, v27, s[2:3]
	v_cndmask_b32_e64 v11, v37, v29, s[2:3]
	v_mov_b32_e32 v42, v47
	v_cndmask_b32_e64 v15, v138, v136, s[2:3]
	v_cndmask_b32_e64 v17, v31, v165, s[2:3]
	v_pk_mul_f32 v[30:31], v[130:131], v[138:139]
	v_pk_fma_f32 v[46:47], v[46:47], v[136:137], v[130:131]
	v_cndmask_b32_e64 v131, v27, v23, s[2:3]
	v_fmac_f32_e32 v124, v126, v12
	v_cvt_pk_bf16_f32 v1, v1, v124
	v_mul_f32_e32 v23, v134, v3
	v_mul_f32_e32 v29, v126, v3
	v_fmac_f32_e32 v34, v16, v12
	v_fmac_f32_e32 v35, v18, v12
	v_mul_f32_e32 v12, v16, v3
	v_mul_f32_e32 v3, v18, v3
	v_cvt_pk_bf16_f32 v23, v23, v29
	ds_write_b16 v187, v1 offset:64
	ds_write_b16_d16_hi v187, v1 offset:192
	ds_write_b16 v187, v23 offset:4160
	ds_write_b16_d16_hi v187, v23 offset:4288
	v_cvt_pk_bf16_f32 v1, v34, v35
	v_cvt_pk_bf16_f32 v3, v12, v3
	v_fmac_f32_e32 v5, v2, v11
	v_mul_f32_e32 v2, v2, v15
	v_cndmask_b32_e64 v132, v21, v26, s[2:3]
	v_mov_b32_e32 v31, v47
	ds_write_b16 v187, v1 offset:320
	ds_write_b16_d16_hi v187, v1 offset:448
	ds_write_b16 v187, v3 offset:4416
	ds_write_b16_d16_hi v187, v3 offset:4544
	v_fmac_f32_e32 v36, v10, v11
	v_cvt_pk_bf16_f32 v1, v5, v36
	v_mul_f32_e32 v3, v10, v15
	v_cvt_pk_bf16_f32 v2, v2, v3
	v_pk_mul_f32 v[136:137], v[132:133], v[30:31]
	ds_write_b16 v187, v1 offset:1088
	ds_write_b16_d16_hi v187, v1 offset:1216
	ds_write_b16 v187, v2 offset:5184
	ds_write_b16_d16_hi v187, v2 offset:5312
	v_mul_f32_e32 v2, v20, v15
	v_cndmask_b32_e64 v43, v0, v44, s[2:3]
	v_cndmask_b32_e64 v19, v136, v30, s[2:3]
	v_fmac_f32_e32 v40, v20, v11
	v_fmac_f32_e32 v4, v22, v11
	v_cvt_pk_bf16_f32 v1, v40, v4
	v_mul_f32_e32 v3, v22, v15
	v_cvt_pk_bf16_f32 v2, v2, v3
	v_pk_mul_f32 v[136:137], v[42:43], v[136:137]
	v_pk_fma_f32 v[30:31], v[132:133], v[30:31], v[42:43]
	ds_write_b16 v187, v1 offset:1344
	ds_write_b16_d16_hi v187, v1 offset:1472
	ds_write_b16 v187, v2 offset:5440
	ds_write_b16_d16_hi v187, v2 offset:5568
	v_mul_f32_e32 v2, v6, v19
	v_mov_b32_e32 v130, v133
	v_mov_b32_e32 v137, v31
	v_fmac_f32_e32 v9, v6, v17
	v_fmac_f32_e32 v128, v24, v17
	v_cvt_pk_bf16_f32 v1, v9, v128
	v_mul_f32_e32 v3, v24, v19
	v_cvt_pk_bf16_f32 v2, v2, v3
	v_cndmask_b32_e64 v139, v44, v0, s[2:3]
	v_cndmask_b32_e64 v0, v31, v47, s[2:3]
	v_pk_mul_f32 v[30:31], v[130:131], v[136:137]
	ds_write_b16 v187, v1 offset:2112
	ds_write_b16_d16_hi v187, v1 offset:2240
	ds_write_b16 v187, v2 offset:6208
	ds_write_b16_d16_hi v187, v2 offset:6336
	v_mul_f32_e32 v2, v38, v19
	v_cndmask_b32_e64 v21, v30, v136, s[2:3]
	v_fmac_f32_e32 v8, v38, v17
	v_fmac_f32_e32 v33, v26, v17
	v_cvt_pk_bf16_f32 v1, v8, v33
	v_mul_f32_e32 v3, v26, v19
	v_cvt_pk_bf16_f32 v2, v2, v3
	ds_write_b16 v187, v1 offset:2368
	ds_write_b16_d16_hi v187, v1 offset:2496
	ds_write_b16 v187, v2 offset:6464
	ds_write_b16_d16_hi v187, v2 offset:6592
	v_fmac_f32_e32 v13, v7, v0
	v_fmac_f32_e32 v28, v25, v0
	v_cvt_pk_bf16_f32 v1, v13, v28
	v_mul_f32_e32 v2, v7, v21
	v_mul_f32_e32 v3, v25, v21
	v_cvt_pk_bf16_f32 v2, v2, v3
	ds_write_b16 v187, v1 offset:3136
	ds_write_b16_d16_hi v187, v1 offset:3264
	ds_write_b16 v187, v2 offset:7232
	ds_write_b16_d16_hi v187, v2 offset:7360
	v_fmac_f32_e32 v14, v39, v0
	v_fmac_f32_e32 v44, v27, v0
	v_cvt_pk_bf16_f32 v0, v14, v44
	v_mul_f32_e32 v1, v39, v21
	v_mul_f32_e32 v2, v27, v21
	v_cvt_pk_bf16_f32 v1, v1, v2
	ds_write_b16 v187, v0 offset:3392
	ds_write_b16_d16_hi v187, v0 offset:3520
	ds_write_b16 v187, v1 offset:7488
	ds_write_b16_d16_hi v187, v1 offset:7616
	s_waitcnt lgkmcnt(0)
	ds_read_b128 v[0:3], v189
	ds_read_b128 v[4:7], v189 offset:4096
	v_lshl_add_u64 v[8:9], s[8:9], 0, v[156:157]
	v_add_co_u32_e32 v10, vcc, s50, v8
	v_mov_b32_e32 v138, v131
	s_nop 0
	v_addc_co_u32_e32 v11, vcc, 0, v9, vcc
	s_waitcnt lgkmcnt(1)
	global_store_dwordx4 v[10:11], v[0:3], off
	v_pk_mul_f32 v[164:165], v[138:139], v[30:31]
	v_pk_fma_f32 v[166:167], v[130:131], v[136:137], v[138:139]
	v_add_co_u32_e32 v0, vcc, s51, v8
	v_lshl_add_u64 v[156:157], v[156:157], 0, s[90:91]
	s_nop 0
	v_addc_co_u32_e32 v1, vcc, 0, v9, vcc
	s_waitcnt lgkmcnt(0)
	global_store_dwordx4 v[0:1], v[4:7], off
	ds_read_b128 v[0:3], v191
	ds_read_b128 v[4:7], v191 offset:4096
	v_lshl_add_u64 v[8:9], s[8:9], 0, v[162:163]
	v_add_co_u32_e32 v10, vcc, s50, v8
	v_lshl_add_u64 v[162:163], v[162:163], 0, s[90:91]
	s_nop 0
	v_addc_co_u32_e32 v11, vcc, 0, v9, vcc
	s_waitcnt lgkmcnt(1)
	global_store_dwordx4 v[10:11], v[0:3], off
	s_nop 1
	v_add_co_u32_e32 v0, vcc, s51, v8
	s_nop 1
	v_addc_co_u32_e32 v1, vcc, 0, v9, vcc
	s_waitcnt lgkmcnt(0)
	global_store_dwordx4 v[0:1], v[4:7], off
	ds_read_b128 v[0:3], v195
	ds_read_b128 v[4:7], v195 offset:4096
	v_lshl_add_u64 v[8:9], s[8:9], 0, v[160:161]
	v_add_co_u32_e32 v10, vcc, s50, v8
	v_lshl_add_u64 v[160:161], v[160:161], 0, s[90:91]
	s_nop 0
	v_addc_co_u32_e32 v11, vcc, 0, v9, vcc
	s_waitcnt lgkmcnt(1)
	global_store_dwordx4 v[10:11], v[0:3], off
	s_nop 1
	v_add_co_u32_e32 v0, vcc, s51, v8
	s_nop 1
	v_addc_co_u32_e32 v1, vcc, 0, v9, vcc
	s_waitcnt lgkmcnt(0)
	global_store_dwordx4 v[0:1], v[4:7], off
	ds_read_b128 v[0:3], v197
	ds_read_b128 v[4:7], v197 offset:4096
	v_lshl_add_u64 v[8:9], s[8:9], 0, v[158:159]
	v_add_co_u32_e32 v10, vcc, s50, v8
	v_lshl_add_u64 v[158:159], v[158:159], 0, s[90:91]
	s_nop 0
	v_addc_co_u32_e32 v11, vcc, 0, v9, vcc
	s_waitcnt lgkmcnt(1)
	global_store_dwordx4 v[10:11], v[0:3], off
	s_nop 1
	v_add_co_u32_e32 v0, vcc, s51, v8
	s_nop 1
	v_addc_co_u32_e32 v1, vcc, 0, v9, vcc
	s_waitcnt lgkmcnt(0)
	global_store_dwordx4 v[0:1], v[4:7], off
	s_cbranch_scc1 .LBB0_631

; #define LAS __attribute__((address_space(3)))
; __device__ __forceinline__ CJob moe_job(KP P, int j2, int j) {
;     CJob jb; jb.pad = 0; jb.gain = nullptr; jb.mode = 0; jb.fp8 = MOE_FP8 ? 1 : 0; jb.wscale = 1.f; jb.col0 = 0; const int e = j / 3, k = j % 3;
;     if (k < 2) { jb.W = P->in[24 + k] + ((size_t)j2 * NEXP + e) * DM * DFF; jb.gain = P->in[18] + (2 * j2 + 1) * DM; jb.dst = (bf16*)(P->ws + WS_W13E + (size_t)e * 2 * DFF * DM * (MOE_FP8 ? 1 : 2)); jb.K = DM; jb.N = DFF; jb.mode = 4 + k; jb.wscale = MOE_FP8 ? W13_SCALE : 1.f; }
;     else { jb.W = P->in[26] + ((size_t)j2 * NEXP + e) * DFF * DM; jb.dst = (bf16*)(P->ws + WS_W2E + (size_t)e * DM * DFF * (MOE_FP8 ? 1 : 2)); jb.K = DFF; jb.N = DM; jb.wscale = MOE_FP8 ? W2_SCALE : 1.f; }
;     jb.ldw = jb.N;
; __device__ __forceinline__ void conv_moe_layer(KP P, int j2, LAS float* scr, int gw, int ngw, int lane) {
;     constexpr int IT = (DM / 64) * (DFF / 32), NT = 24 * IT;
;     int fl = gw; if (fl >= NT) return;
;     CJob jb = moe_job(P, j2, fl / IT); f32x4 v[8]; conv_load(jb, fl % IT, lane, v);
.LBB0_646:
	s_lshl_b32 s8, s2, 11
	s_mov_b32 s9, s40
	s_mul_hi_u32 s1, s2, 0x7000000
	s_andn2_b64 vcc, exec, s[16:17]
	s_mul_i32 s22, s2, 0x7000000
	s_cbranch_vccnz .LBB0_648
	s_ashr_i32 s15, s14, 31
	s_lshl_b32 s3, s14, 1
	s_add_i32 s3, s3, 49
	v_readlane_b32 s2, v255, s3
	s_add_i32 s3, s3, 1
	v_readlane_b32 s3, v255, s3
	s_mul_i32 s11, s20, 0xe00000
	s_mul_hi_i32 s10, s20, 0xe00000
	s_mul_hi_i32 s15, s20, 0x700000
	s_mul_i32 s20, s20, 0x700000
	s_waitcnt lgkmcnt(0)
	s_add_u32 s2, s2, s11
	s_addc_u32 s3, s3, s10
	s_add_u32 s10, s2, s22
	s_addc_u32 s11, s3, s1
	v_readlane_b32 s2, v255, 55
	v_readlane_b32 s3, v255, 56
	s_lshl_b64 s[12:13], s[8:9], 2
	s_mov_b32 s24, 0x42800000
	s_movk_i32 s33, 0xe00
	s_movk_i32 s23, 0x400
	s_add_u32 s2, s2, s12
	s_addc_u32 s3, s3, s13
	s_mov_b64 s[12:13], s[100:101]
	s_add_u32 s2, s2, 0x1000
	s_addc_u32 s3, s3, 0
	s_add_u32 s12, s12, s20
	s_addc_u32 s13, s13, s15
	s_add_u32 s12, s12, 0x7a00000
	s_addc_u32 s13, s13, 0
	s_add_i32 s30, s14, 4
	s_branch .LBB0_649

; __device__ __forceinline__ CJob moe_job(KP P, int j2, int j) {
;     CJob jb; jb.pad = 0; jb.gain = nullptr; jb.mode = 0; jb.fp8 = MOE_FP8 ? 1 : 0; jb.wscale = 1.f; jb.col0 = 0; const int e = j / 3, k = j % 3;
;     if (k < 2) { jb.W = P->in[24 + k] + ((size_t)j2 * NEXP + e) * DM * DFF; jb.gain = P->in[18] + (2 * j2 + 1) * DM; jb.dst = (bf16*)(P->ws + WS_W13E + (size_t)e * 2 * DFF * DM * (MOE_FP8 ? 1 : 2)); jb.K = DM; jb.N = DFF; jb.mode = 4 + k; jb.wscale = MOE_FP8 ? W13_SCALE : 1.f; }
;     else { jb.W = P->in[26] + ((size_t)j2 * NEXP + e) * DFF * DM; jb.dst = (bf16*)(P->ws + WS_W2E + (size_t)e * DM * DFF * (MOE_FP8 ? 1 : 2)); jb.K = DFF; jb.N = DM; jb.wscale = MOE_FP8 ? W2_SCALE : 1.f; }
;     jb.ldw = jb.N;
; __device__ __forceinline__ void conv_moe_layer(KP P, int j2, LAS float* scr, int gw, int ngw, int lane) {
;     ...
;     for (;;) { const int nx = fl + ngw; const bool has = nx < NT; CJob jn = jb; f32x4 w[8];
;         if (has) { jn = moe_job(P, j2, nx / IT); conv_load(jn, nx % IT, lane, w); }
.LBB0_654:
	s_andn2_b64 vcc, exec, s[14:15]
	s_cbranch_vccnz .LBB0_656
	s_ashr_i32 s21, s20, 31
	s_lshl_b32 s11, s20, 1
	s_add_i32 s11, s11, 49
	v_readlane_b32 s10, v255, s11
	s_add_i32 s11, s11, 1
	v_readlane_b32 s11, v255, s11
	s_mul_i32 s15, s26, 0xe00000
	s_mul_hi_i32 s14, s26, 0xe00000
	s_mul_hi_i32 s21, s26, 0x700000
	s_mul_i32 s26, s26, 0x700000
	s_waitcnt lgkmcnt(0)
	s_add_u32 s10, s10, s15
	s_addc_u32 s11, s11, s14
	v_readlane_b32 s14, v255, 55
	v_readlane_b32 s15, v255, 56
	s_add_u32 s10, s10, s22
	s_addc_u32 s11, s11, s1
	s_lshl_b64 s[16:17], s[8:9], 2
	s_mov_b32 s27, 0x42800000
	s_add_u32 s14, s14, s16
	s_addc_u32 s15, s15, s17
	s_mov_b64 s[16:17], s[100:101]
	s_add_u32 s14, s14, 0x1000
	s_addc_u32 s15, s15, 0
	s_movk_i32 s28, 0xe00
	s_movk_i32 s29, 0x400
	s_add_u32 s16, s16, s26
	s_addc_u32 s17, s17, s21
	s_add_u32 s16, s16, 0x7a00000
	s_addc_u32 s17, s17, 0
	s_add_i32 s26, s20, 4
	s_branch .LBB0_657

; #define LAS __attribute__((address_space(3)))
; __device__ __forceinline__ unsigned cvt_pk_bf16(float lo, float hi) { unsigned r; asm volatile("v_cvt_pk_bf16_f32 %0, %1, %2" : "=v"(r) : "v"(lo), "v"(hi)); return r; }
; __device__ __forceinline__ void conv_finish(const CJob& jb, LAS float* scr, int item, int lane, const f32x4 (&v)[8]) {
;     ...
;     for (int j = 0; j < 4; ++j) { const int n = (lane >> 3) + 8 * j; const LAS float* s = scr + (8 * c) * 33 + n;
;         u32x4 o; o.x = cvt_pk_bf16(s[0 * 33] * g0.x, s[1 * 33] * g0.y); o.y = cvt_pk_bf16(s[2 * 33] * g0.z, s[3 * 33] * g0.w); o.z = cvt_pk_bf16(s[4 * 33] * g1.x, s[5 * 33] * g1.y); o.w = cvt_pk_bf16(s[6 * 33] * g1.z, s[7 * 33] * g1.w);
;         const int nn = n0 + n; int row = nn;
;         if (jb.mode == 3) { const int w = nn & 255; row = (nn & ~255) + ((w >> 5) & 1) * 128 + (w >> 6) * 32 + (w & 31); }
;         else if (jb.mode >= 4) { const int r = nn & 127; row = (nn >> 7) * 256 + ((r >> 2) & 1) * 128 + (r >> 5) * 32 + ((r >> 3) & 3) * 8 + (jb.mode == 5 ? 4 : 0) + (r & 3); }
;         if (jb.fp8) { const float ws_ = jb.wscale; u32x2 o8; o8.x = pk4_fp8(s[0 * 33] * g0.x * ws_, s[1 * 33] * g0.y * ws_, s[2 * 33] * g0.z * ws_, s[3 * 33] * g0.w * ws_);
;             o8.y = pk4_fp8(s[4 * 33] * g1.x * ws_, s[5 * 33] * g1.y * ws_, s[6 * 33] * g1.z * ws_, s[7 * 33] * g1.w * ws_); *(u32x2*)((unsigned char*)jb.dst + (size_t)row * jb.K + k0 + 8 * c) = o8; }
;         else *(u32x4*)(jb.dst + (size_t)row * jb.K + k0 + 8 * c) = o; }
;     asm volatile("s_waitcnt lgkmcnt(0)" ::: "memory");
; }
; __device__ __forceinline__ void conv_moe_layer(KP P, int j2, LAS float* scr, int gw, int ngw, int lane) {
;     ...
;         conv_finish(jb, scr, fl % IT, lane, v);
;         if (!has) break;
;         jb = jn; fl = nx;
; #pragma unroll
;         for (int i = 0; i < 8; ++i) v[i] = w[i]; }
.LBB0_677:
	ds_read2_b32 v[34:35], v79 offset0:24 offset1:57
	s_andn2_b64 vcc, exec, s[18:19]
	s_waitcnt lgkmcnt(0)
	v_mul_f32_e32 v32, v68, v34
	v_mul_f32_e32 v34, v69, v35
	v_mul_f32_e32 v36, s24, v34
	ds_read2_b32 v[34:35], v79 offset0:90 offset1:123
	v_mul_f32_e32 v32, s24, v32
	s_waitcnt lgkmcnt(0)
	v_mul_f32_e32 v34, v70, v34
	v_mul_f32_e32 v37, s24, v34
	v_mul_f32_e32 v34, v71, v35
	v_mul_f32_e32 v35, s24, v34
	v_med3_f32 v34, v32, s49, v254
	v_med3_f32 v32, v36, s49, v254
	v_cvt_pk_fp8_f32 v34, v34, v32
	v_med3_f32 v36, v37, s49, v254
	v_med3_f32 v35, v35, s49, v254
	v_cvt_pk_fp8_f32 v34, v36, v35 op_sel:[0,0,1]
	ds_read2_b32 v[36:37], v79 offset0:156 offset1:189
	s_waitcnt lgkmcnt(0)
	v_mul_f32_e32 v32, v64, v36
	v_mul_f32_e32 v35, v65, v37
	ds_read2_b32 v[36:37], v79 offset0:222 offset1:255
	v_mul_f32_e32 v38, s24, v35
	v_mul_f32_e32 v32, s24, v32
	s_waitcnt lgkmcnt(0)
	v_mul_f32_e32 v35, v66, v36
	v_mul_f32_e32 v36, s24, v35
	v_mul_f32_e32 v35, v67, v37
	v_mul_f32_e32 v37, s24, v35
	v_med3_f32 v35, v32, s49, v254
	v_med3_f32 v32, v38, s49, v254
	v_cvt_pk_fp8_f32 v35, v35, v32
	v_med3_f32 v36, v36, s49, v254
	v_med3_f32 v37, v37, s49, v254
	v_ashrrev_i32_e32 v38, 31, v33
	v_cvt_pk_fp8_f32 v35, v36, v37 op_sel:[0,0,1]
	v_mov_b64_e32 v[36:37], s[12:13]
	v_mad_u64_u32 v[32:33], s[2:3], v33, s23, v[36:37]
	v_mov_b32_e32 v36, v33
	v_mad_u64_u32 v[36:37], s[2:3], v38, s23, v[36:37]
	v_mov_b32_e32 v33, v36
	v_lshl_add_u64 v[32:33], v[32:33], 0, s[10:11]
	v_lshl_add_u64 v[32:33], v[32:33], 0, v[72:73]
	global_store_dwordx2 v[32:33], v[34:35], off
	s_mov_b64 s[2:3], -1
	s_cbranch_vccnz .LBB0_650
	s_mov_b64 s[2:3], 0
	v_mov_b32_e32 v35, v27
	v_mov_b32_e32 v34, v26
	v_mov_b32_e32 v33, v25
	v_mov_b32_e32 v32, v24
	v_mov_b32_e32 v39, v31
	v_mov_b32_e32 v38, v30
	v_mov_b32_e32 v37, v29
	v_mov_b32_e32 v36, v28
	v_mov_b32_e32 v43, v19
	v_mov_b32_e32 v42, v18
	v_mov_b32_e32 v41, v17
	v_mov_b32_e32 v40, v16
	v_mov_b32_e32 v47, v23
	v_mov_b32_e32 v46, v22
	v_mov_b32_e32 v45, v21
	v_mov_b32_e32 v44, v20
	v_mov_b32_e32 v51, v11
	v_mov_b32_e32 v50, v10
	v_mov_b32_e32 v49, v9
	v_mov_b32_e32 v48, v8
	v_mov_b32_e32 v55, v15
	v_mov_b32_e32 v54, v14
	v_mov_b32_e32 v53, v13
	v_mov_b32_e32 v52, v12
	v_mov_b32_e32 v59, v3
	v_mov_b32_e32 v58, v2
	v_mov_b32_e32 v57, v1
	v_mov_b32_e32 v56, v0
	v_mov_b32_e32 v63, v7
	v_mov_b32_e32 v62, v6
	v_mov_b32_e32 v61, v5
	v_mov_b32_e32 v60, v4
	s_branch .LBB0_650

; __device__ __forceinline__ int opaque_tid(int wbase) { int t = wbase + lane_id(); asm volatile("" : "+v"(t)); return t; }
; __device__ __forceinline__ int opaque_s(int x) { asm volatile("" : "+s"(x)); return x; }
; #define KWS (kargs()->ws)
; template <bool F8> __device__ __forceinline__ void lru_apply(const bf16* U, const bf16* HR, const bf16* PQ, const float* AGG, bf16* YB, int G, int c, int wbase) {
;     const int tid = opaque_tid(wbase); G = opaque_s(G); c = opaque_s(c); const int ch = 8 * (tid & 127), tq = tid >> 7;
;     for (int cu = c; cu < BATCH * NCK; cu += G) { const int b = cu / NCK, ck = cu % NCK;
; __global__ void __launch_bounds__(512, 2) mega(Ptrs Pdummy) {
;     ...
;         if ((MERGE_FP8_MASK >> opaque_s(l)) & 1) { unsigned char* ws = KWS; lru::lru_apply<true>((const bf16*)(ws + WS_R + R_U), (const bf16*)(ws + WS_R + R_HR), (const bf16*)(ws + WS_R + R_PQ), (const float*)(ws + WS_AGG), (bf16*)(ws + WS_R + R_YB), G, c, wbase); }
.LBB0_723:
	s_or_b64 exec, exec, s[36:37]
	s_mov_b32 s1, s95
	s_waitcnt lgkmcnt(0)
	s_barrier
	s_lshl_b32 s1, 1, s1
	s_and_b32 s1, s1, 14
	s_cmp_eq_u32 s1, 0
	s_cbranch_scc1 .LBB0_737
	s_mov_b64 s[2:3], s[88:89]
	s_mov_b32 s1, s38
	v_readlane_b32 s4, v255, 4
	v_mbcnt_lo_u32_b32 v0, s1, 0
	v_mbcnt_hi_u32_b32 v0, s1, v0
	v_add_u32_e32 v0, s93, v0
	s_mov_b32 s1, s4
	s_mov_b32 s8, s92
	s_cmpk_gt_i32 s8, 0xff
	v_readlane_b32 s5, v255, 5
	s_cbranch_scc1 .LBB0_736
	s_mov_b64 s[2:3], s[100:101]
	v_and_b32_e32 v2, 0x7f, v0
	v_lshlrev_b32_e32 v1, 3, v0
	v_lshlrev_b32_e32 v232, 6, v2
	v_ashrrev_i32_e32 v53, 7, v0
	v_and_b32_e32 v52, 0x3f8, v1
	v_lshl_add_u64 v[0:1], s[2:3], 0, v[232:233]
	s_mov_b64 s[4:5], 0x1760e030
	v_lshl_add_u64 v[54:55], v[0:1], 0, s[4:5]
	s_mov_b64 s[4:5], 0x17600000
	v_lshl_add_u64 v[56:57], v[0:1], 0, s[4:5]
	v_lshlrev_b32_e32 v58, 4, v2

; #define LAS __attribute__((address_space(3)))
; __device__ __forceinline__ int opaque_tid(int wbase) { int t = wbase + lane_id(); asm volatile("" : "+v"(t)); return t; }
; __device__ __forceinline__ int opaque_s(int x) { asm volatile("" : "+s"(x)); return x; }
; template <int MASK> __device__ __forceinline__ int swz_i(int v) { return __builtin_amdgcn_ds_swizzle(v, (MASK << 10) | 0x1f); }
; __device__ __forceinline__ int sum_x32i(int v) { auto rr = __builtin_amdgcn_permlane32_swap((unsigned)v, (unsigned)v, false, false); return (int)rr[0] + (int)rr[1]; }
; __device__ __forceinline__ void route_b(LAS unsigned char* lds, const int* sel, const float* selw, const float* ssq, const int* CNT, const bf16* hb, int* tok, float* srs, float* sgw, int* tslot, int* meta, bf16* XG, int G, int c, int wbase) {
;     const int tid = opaque_tid(wbase), lane = tid & 63, wid = __builtin_amdgcn_readfirstlane(tid >> 6); G = opaque_s(G); c = opaque_s(c);
;     LAS int* tot = (LAS int*)lds; LAS int* pre = tot + 8; LAS int* start = tot + 16; LAS int* pos = tot + 32; LAS float* rsl = (LAS float*)(tot + 32 + 256);
;     for (int chunk = c; chunk < NCHUNK; chunk += G) {
;         { int t = 0, p = 0;
; #pragma unroll
;           for (int j = 0; j < NCHUNK / 64; ++j) { const int ch = lane + 64 * j; const int v = CNT[ch * 8 + wid]; t += v; p += (ch < chunk) ? v : 0; }
;           t += swz_i<1>(t); t += swz_i<2>(t); t += swz_i<4>(t); t += swz_i<8>(t); t += swz_i<16>(t); t = sum_x32i(t);
;           p += swz_i<1>(p); p += swz_i<2>(p); p += swz_i<4>(p); p += swz_i<8>(p); p += swz_i<16>(p); p = sum_x32i(p);
;           if (lane == 0) { tot[wid] = t; pre[wid] = p; } }
.LBB0_1163:
	s_or_b64 exec, exec, s[10:11]
	s_mov_b64 s[2:3], s[88:89]
	s_mov_b32 s1, s38
	s_waitcnt lgkmcnt(0)
	s_barrier
	v_readlane_b32 s4, v255, 4
	v_mbcnt_lo_u32_b32 v0, s1, 0
	v_mbcnt_hi_u32_b32 v0, s1, v0
	v_add_u32_e32 v12, s93, v0
	s_mov_b32 s1, s4
	s_mov_b32 s30, s92
	s_cmpk_lt_i32 s30, 0x100
	v_readfirstlane_b32 s22, v12
	v_readlane_b32 s5, v255, 5
	s_cbranch_scc0 .LBB0_1267
	s_mov_b64 s[24:25], s[100:101]
	v_readlane_b32 s2, v255, 11
	s_cmp_eq_u32 s2, 1
	s_cselect_b32 s2, 0, 0x200000
	v_and_b32_e32 v17, 63, v12
	s_add_u32 s8, s24, 0x17600000
	s_addc_u32 s9, s25, 0
	s_add_u32 s10, s24, 0x17640000
	s_addc_u32 s11, s25, 0
	s_add_u32 s2, s24, s2
	s_addc_u32 s3, s25, 0
	s_add_u32 s12, s2, 0x17200000
	s_addc_u32 s13, s3, 0
	s_add_u32 s14, s24, 0x17700000
	s_addc_u32 s15, s25, 0
	s_add_u32 s16, s24, 0x17750000
	s_addc_u32 s17, s25, 0
	s_add_u32 s18, s24, 0x177a0000
	s_addc_u32 s19, s25, 0
	s_add_u32 s20, s24, 0x17680000
	s_addc_u32 s21, s25, 0
	s_ashr_i32 s31, s22, 6
	v_readlane_b32 s2, v255, 10
	s_cmp_eq_u32 s2, 0
	s_mov_b32 s2, 0x13200000
	s_cselect_b32 s2, s2, 0x1b800000
	s_add_u32 s26, s24, s2
	v_ashrrev_i32_e32 v13, 31, v12
	s_addc_u32 s27, s25, 0
	v_lshl_add_u64 v[0:1], v[12:13], 2, s[24:25]
	s_mov_b64 s[34:35], 0x177f0000
	v_lshlrev_b32_e32 v232, 5, v17
	s_add_u32 s28, s24, 0x177f1000
	v_lshl_add_u64 v[14:15], v[0:1], 0, s[34:35]
	v_lshlrev_b64 v[0:1], v12, -1
	v_lshl_add_u64 v[18:19], s[26:27], 0, v[232:233]
	v_lshlrev_b32_e32 v232, 4, v17
	s_addc_u32 s29, s25, 0
	v_not_b32_e32 v13, v1
	v_not_b32_e32 v16, v0
	v_lshl_add_u64 v[0:1], s[24:25], 0, v[232:233]
	s_mov_b64 s[24:25], 0x1f800000
	v_lshl_add_u64 v[20:21], v[0:1], 0, s[24:25]
	v_lshl_add_u32 v0, v17, 3, s31
	v_ashrrev_i32_e32 v1, 31, v0
	v_or_b32_e32 v41, 64, v17
	s_lshl_b32 s4, s31, 2
	v_lshl_add_u64 v[22:23], v[0:1], 2, s[28:29]
	v_lshl_add_u32 v0, v41, 3, s31
	s_add_i32 s33, s4, 0
	v_ashrrev_i32_e32 v1, 31, v0
	v_or_b32_e32 v42, 0x80, v17
	s_cmp_gt_u32 s22, 63
	v_lshl_add_u64 v[24:25], v[0:1], 2, s[28:29]
	v_lshl_add_u32 v0, v42, 3, s31
	s_cselect_b64 s[22:23], -1, 0
	s_lshl_b32 s34, s31, 5
	v_ashrrev_i32_e32 v1, 31, v0
	v_or_b32_e32 v43, 0xc0, v17
	s_lshl_b32 s24, s31, 7
	v_lshl_add_u64 v[26:27], v[0:1], 2, s[28:29]
	v_lshl_add_u32 v0, v43, 3, s31
	s_add_i32 s36, s24, 0
	s_lshl_b32 s24, s30, 7
	s_and_b32 s25, s34, 32
	v_ashrrev_i32_e32 v1, 31, v0
	s_or_b32 s24, s24, s25
	v_cmp_eq_u32_e64 s[2:3], 0, v17
	v_cmp_eq_u32_e64 s[4:5], 0, v12
	v_cmp_gt_i32_e64 s[6:7], 9, v12
	v_lshl_add_u32 v40, v12, 2, 0
	v_lshl_add_u64 v[28:29], v[0:1], 2, s[28:29]
	v_lshl_add_u32 v44, v17, 2, 0
	s_or_b32 s35, s34, 28
	v_not_b32_e32 v45, v12
	v_add_u32_e32 v46, 0x200, v12
	s_addk_i32 s36, 0x80
	s_or_b32 s37, s24, 3
	s_lshl_b32 s44, s1, 7
	s_branch .LBB0_1166

;     __device__ __forceinline__ bool next(int i, Unit& u) const { return so.next(i, u); }
;     __device__ __forceinline__ void setup(int G_, int c_) { so.setup(G_, c_); }
;     __device__ __forceinline__ bool next(int i, Unit& u) const { const bool ok = so.next(i >> 1, u); u.part = i & 1; return ok; }
;     __host__ __device__ bool next(int i, Unit& u) const {
;         const int L = i * G + c; if (L >= nwg) return false;
;         int wgid = L; { const int q = nwg / NXCD, r = nwg % NXCD, xcd = wgid % NXCD, off = wgid / NXCD; wgid = (xcd < r ? xcd * (q + 1) : r * (q + 1) + (xcd - r) * q) + off; }
;     __device__ __forceinline__ void setup(int G_, int c_) {
; #pragma unroll
;         for (int e = 0; e < 9; ++e) ts[e] = __builtin_amdgcn_readfirstlane(__hip_atomic_load(meta + e, __ATOMIC_RELAXED, __HIP_MEMORY_SCOPE_AGENT));
;         so.init(ts[8] * BM, N, G_, c_);
.LBB0_1312:
	s_or_b64 exec, exec, s[10:11]
	s_mov_b64 s[2:3], s[88:89]
	s_waitcnt lgkmcnt(0)
	s_barrier
	s_mov_b64 s[2:3], s[100:101]
	v_readlane_b32 s4, v255, 4
	s_mov_b32 s1, s4
	s_mov_b32 s22, s92
	v_mov_b32_e32 v1, 0x177f0000
	global_load_dword v0, v1, s[2:3] sc1
	global_load_dword v33, v1, s[2:3] offset:4 sc1
	global_load_dword v34, v1, s[2:3] offset:8 sc1
	global_load_dword v35, v1, s[2:3] offset:12 sc1
	global_load_dword v36, v1, s[2:3] offset:16 sc1
	global_load_dword v37, v1, s[2:3] offset:20 sc1
	global_load_dword v38, v1, s[2:3] offset:24 sc1
	global_load_dword v39, v1, s[2:3] offset:28 sc1
	global_load_dword v40, v1, s[2:3] offset:32 sc1
	s_mov_b32 s4, s38
	s_movk_i32 s16, 0x200
	v_readlane_b32 s5, v255, 5
	s_waitcnt vmcnt(0)
	v_readfirstlane_b32 s23, v33
	v_readfirstlane_b32 s24, v34
	v_readfirstlane_b32 s25, v35
	v_readfirstlane_b32 s26, v36
	v_readfirstlane_b32 s27, v37
	v_readfirstlane_b32 s28, v38
	v_readfirstlane_b32 s29, v39
	v_readfirstlane_b32 s30, v40
	v_mbcnt_lo_u32_b32 v0, s4, 0
	v_mbcnt_hi_u32_b32 v0, s4, v0
	s_mul_i32 s31, s30, 28
	v_add_u32_e32 v1, s93, v0
	s_cmp_lt_i32 s22, s31
	v_readfirstlane_b32 s15, v1
	s_cbranch_scc0 .LBB0_1372
	s_ashr_i32 s4, s31, 31
	s_lshr_b32 s4, s4, 29
	s_add_i32 s4, s31, s4
	s_ashr_i32 s33, s4, 3
	s_and_b32 s4, s4, -8
	s_sub_i32 s34, s31, s4
	s_ashr_i32 s4, s22, 31
	s_lshr_b32 s4, s4, 29
	s_add_i32 s7, s22, s4
	s_and_b32 s4, s7, -8
	s_sub_i32 s8, s22, s4
	s_add_i32 s35, s33, 1
	s_cmp_ge_i32 s8, s34
	s_mov_b64 s[4:5], -1
	s_cbranch_scc0 .LBB0_1315
	s_sub_i32 s5, s8, s34
	s_mul_i32 s4, s35, s34
	s_mul_i32 s5, s5, s33
	s_add_i32 s6, s4, s5
	s_mov_b64 s[4:5], 0

;     __device__ __forceinline__ bool next(int i, Unit& u) const { return so.next(i, u); }
;     __device__ __forceinline__ void setup(int G_, int c_) { so.setup(G_, c_); }
;     __device__ __forceinline__ bool next(int i, Unit& u) const { const bool ok = so.next(i >> 1, u); u.part = i & 1; return ok; }
;     __host__ __device__ bool next(int i, Unit& u) const {
;         const int L = i * G + c; if (L >= nwg) return false;
;         int wgid = L; { const int q = nwg / NXCD, r = nwg % NXCD, xcd = wgid % NXCD, off = wgid / NXCD; wgid = (xcd < r ? xcd * (q + 1) : r * (q + 1) + (xcd - r) * q) + off; }
;     __device__ __forceinline__ void setup(int G_, int c_) {
; #pragma unroll
;         for (int e = 0; e < 9; ++e) ts[e] = __builtin_amdgcn_readfirstlane(__hip_atomic_load(meta + e, __ATOMIC_RELAXED, __HIP_MEMORY_SCOPE_AGENT));
;         so.init(ts[8] * BM, N, G_, c_);
.LBB0_1417:
	s_or_b64 exec, exec, s[10:11]
	s_mov_b64 s[2:3], s[88:89]
	s_waitcnt lgkmcnt(0)
	s_barrier
	s_mov_b64 s[2:3], s[100:101]
	v_readlane_b32 s4, v255, 4
	s_mov_b32 s1, s4
	s_mov_b32 s20, s92
	v_mov_b32_e32 v1, 0x177f0000
	global_load_dword v0, v1, s[2:3] sc1
	global_load_dword v33, v1, s[2:3] offset:4 sc1
	global_load_dword v34, v1, s[2:3] offset:8 sc1
	global_load_dword v35, v1, s[2:3] offset:12 sc1
	global_load_dword v36, v1, s[2:3] offset:16 sc1
	global_load_dword v37, v1, s[2:3] offset:20 sc1
	global_load_dword v38, v1, s[2:3] offset:24 sc1
	global_load_dword v39, v1, s[2:3] offset:28 sc1
	global_load_dword v40, v1, s[2:3] offset:32 sc1
	s_mov_b32 s4, s38
	s_movk_i32 s12, 0x700
	v_readlane_b32 s5, v255, 5
	s_waitcnt vmcnt(0)
	v_readfirstlane_b32 s21, v33
	v_readfirstlane_b32 s22, v34
	v_readfirstlane_b32 s23, v35
	v_readfirstlane_b32 s24, v36
	v_readfirstlane_b32 s25, v37
	v_readfirstlane_b32 s26, v38
	v_readfirstlane_b32 s27, v39
	v_readfirstlane_b32 s28, v40
	v_mbcnt_lo_u32_b32 v0, s4, 0
	v_mbcnt_hi_u32_b32 v0, s4, v0
	s_lshl_b32 s29, s28, 2
	v_add_u32_e32 v1, s93, v0
	s_cmp_lt_i32 s20, s29
	v_readfirstlane_b32 s14, v1
	s_cbranch_scc0 .LBB0_1477
	s_lshr_b32 s4, s28, 31
	s_add_i32 s4, s28, s4
	s_ashr_i32 s30, s4, 1
	s_ashr_i32 s4, s29, 31
	s_lshr_b32 s4, s4, 29
	s_add_i32 s4, s29, s4
	s_and_b32 s4, s4, -8
	s_sub_i32 s31, s29, s4
	s_ashr_i32 s4, s20, 31
	s_lshr_b32 s4, s4, 29
	s_add_i32 s7, s20, s4
	s_and_b32 s4, s7, -8
	s_sub_i32 s8, s20, s4
	s_add_i32 s33, s30, 1
	s_cmp_ge_i32 s8, s31
	s_mov_b64 s[4:5], -1
	s_cbranch_scc0 .LBB0_1420
	s_sub_i32 s5, s8, s31
	s_mul_i32 s4, s33, s31
	s_mul_i32 s5, s5, s30
	s_add_i32 s6, s5, s4
	s_mov_b64 s[4:5], 0

; #define KWS (kargs()->ws)
; #define WAVE_IDS() const int tid = opaque_tid(wbase), lane = tid & 63, wid = __builtin_amdgcn_readfirstlane(tid >> 6), gw = c * 8 + wid, ngw = G * 8; (void)tid; (void)lane; (void)gw; (void)ngw
; __global__ void __launch_bounds__(512, 2) mega(Ptrs Pdummy) {
;     ...
;             { WAVE_IDS(); unsigned char* ws = KWS; const int* TSLOT = (const int*)(ws + WS_SEL + 512 * 1024); const bf16* XG = (const bf16*)(ws + WS_R + R_XG);
;               for (int m = gw; m < M; m += 2 * ngw) { const int m2 = m + ngw;
;                   if (m2 >= M) { rowstats_row<true>(nullptr, HBUF(hc) + (size_t)m * DM, SBUF(sc ^ 1) + 16 * (size_t)m, XG + (size_t)TSLOT[2 * m] * DM, XG + (size_t)TSLOT[2 * m + 1] * DM, lane); break; }
;                   const int s1 = TSLOT[2 * m], s2 = TSLOT[2 * m + 1], s3 = TSLOT[2 * m2], s4 = TSLOT[2 * m2 + 1];
;                   const bool p8 = (PLE_FP8_MASK >> l) & 1;
;                   combine_rows2(HBUF(hc) + (size_t)m * DM, SBUF(sc ^ 1) + 16 * (size_t)m, XG + (size_t)s1 * DM, XG + (size_t)s2 * DM,
;                                 HBUF(hc) + (size_t)m2 * DM, SBUF(sc ^ 1) + 16 * (size_t)m2, XG + (size_t)s3 * DM, XG + (size_t)s4 * DM, lane,
;                                 p8 ? ws + WS_HB8 + (size_t)m * DM : nullptr, p8 ? ws + WS_HB8 + (size_t)m2 * DM : nullptr); } }
.LBB0_1522:
	s_or_b64 exec, exec, s[10:11]
	s_mov_b32 s1, s38
	s_waitcnt lgkmcnt(0)
	s_barrier
	s_mov_b64 s[2:3], s[88:89]
	v_mbcnt_lo_u32_b32 v0, s1, 0
	v_mbcnt_hi_u32_b32 v0, s1, v0
	v_add_u32_e32 v0, s93, v0
	s_nop 0
	v_readfirstlane_b32 s1, v0
	s_ashr_i32 s8, s1, 6
	v_readlane_b32 s1, v255, 27
	s_add_i32 s10, s8, s1
	s_cmpk_gt_i32 s10, 0x7fff
	s_cbranch_scc1 .LBB0_1571
	s_mov_b64 s[6:7], s[100:101]
	v_readlane_b32 s2, v255, 10
	v_and_b32_e32 v0, 63, v0
	v_readlane_b32 s4, v255, 11
	v_lshlrev_b32_e32 v232, 3, v0
	s_add_u32 s1, s6, 0x17680000
	s_addc_u32 s22, s7, 0
	s_cmp_eq_u32 s2, 0
	s_mov_b32 s2, 0x13200000
	s_cselect_b32 s2, s2, 0x1b800000
	s_add_u32 s2, s6, s2
	s_addc_u32 s3, s7, 0
	s_cmp_eq_u32 s4, 0
	v_lshl_add_u64 v[2:3], s[2:3], 0, v[232:233]
	s_cselect_b32 s2, 0, 0x200000
	s_add_u32 s12, s6, s2
	s_addc_u32 s13, s7, 0
	v_lshl_add_u64 v[4:5], s[6:7], 0, v[232:233]
	v_lshlrev_b32_e32 v232, 2, v0
	s_add_u32 s23, s6, 0xb200000
	s_mov_b64 s[2:3], 0x1f800000
	v_lshl_add_u64 v[6:7], s[12:13], 0, v[232:233]
	s_mov_b64 s[12:13], 0x17200000
	s_addc_u32 s24, s7, 0
	s_lshl_b32 s8, s8, 1
	v_readlane_b32 s9, v255, 3
	v_lshl_add_u64 v[4:5], v[4:5], 0, s[2:3]
	v_cmp_eq_u32_e64 s[2:3], 3, v0
	v_cmp_gt_u32_e64 s[4:5], 16, v0
	v_lshl_add_u64 v[6:7], v[6:7], 0, s[12:13]
	v_cmp_ne_u32_e64 s[6:7], 0, v0
	s_add_i32 s12, s9, s8
	v_lshlrev_b32_e32 v232, 2, v0
	s_branch .LBB0_1526
